# attention: K fp8 to bf16 in one exact convert, V index reads with immediate offsets; DSA classify loop with writelane and prefetched LDS reads
# speedup vs baseline: 1.0050x; 1.0050x over previous
.LBB0_964:
	s_or_b64 exec, exec, s[2:3]
	s_add_i32 s75, s75, 1
	s_lshl_b32 s2, s75, 3
	s_add_i32 s2, s2, 63
	s_lshl_b32 s60, s75, 4
	s_and_b32 s2, s2, 0x7fffffc0
	v_mov_b32_e32 v4, s2
	v_mov_b32_e32 v5, s60
	v_cndmask_b32_e64 v128, v4, 0, s[8:9]
	v_cndmask_b32_e64 v129, v5, v4, s[8:9]
	s_waitcnt lgkmcnt(0)
	s_barrier
	ds_read2_b32 v[122:123], v165 offset1:4
	v_sub_u32_e32 v4, v129, v128
	v_add_u32_e32 v4, 63, v4
	v_mov_b32_e32 v118, 0
	v_ashrrev_i32_e32 v130, 6, v4
	v_cmp_lt_i32_e32 vcc, 0, v130
	v_mov_b32_e32 v119, v118
	v_mov_b32_e32 v4, v118
	v_mov_b32_e32 v5, v118
	s_and_saveexec_b64 s[2:3], vcc
	s_cbranch_execz .LBB0_970
	v_add_u32_e32 v131, v158, v128
	v_mov_b32_e32 v118, 0
	v_lshl_add_u32 v132, v131, 2, v170
	v_mov_b32_e32 v119, v118
	v_mov_b32_e32 v4, v118
	v_mov_b32_e32 v5, v118
	v_readfirstlane_b32 s99, v130
	s_mov_b32 m0, 0
	ds_read_b32 v134, v132
.Ldsa_cmp_loop:
	v_cmp_lt_u32_e32 vcc, v131, v129
	v_add_u32_e32 v132, 0x100, v132
	ds_read_b32 v135, v132
	s_waitcnt lgkmcnt(1)
	v_cndmask_b32_e32 v134, 0, v134, vcc
	v_lshrrev_b32_e32 v136, 21, v134
	v_cmp_eq_u32_e64 s[36:37], v136, v122
	v_cmp_ne_u32_e64 s[38:39], 0, v134
	s_and_b64 s[36:37], s[38:39], s[36:37]
	v_cmp_gt_u32_e32 vcc, v136, v122
	v_add_u32_e32 v131, 64, v131
	s_nop 1
	v_writelane_b32 v118, vcc_lo, m0
	v_writelane_b32 v119, vcc_hi, m0
	v_writelane_b32 v4, s36, m0
	v_writelane_b32 v5, s37, m0
	s_add_i32 m0, m0, 1
	s_cmp_lt_u32 m0, s99
	s_waitcnt lgkmcnt(0)
	v_mov_b32_e32 v134, v135
	s_cbranch_scc1 .Ldsa_cmp_loop

.LBB0_1220:
	s_or_b64 exec, exec, s[2:3]
	v_lshl_add_u64 v[66:67], v[116:117], 0, v[50:51]
	global_load_dwordx4 v[50:53], v[66:67], off offset:16
	s_nop 0
	global_load_dwordx4 v[66:69], v[66:67], off
	s_waitcnt vmcnt(14)
	v_cvt_pk_f32_fp8_e32 v[188:189], v54
	v_cvt_pk_f32_fp8_sdwa v[190:191], v54 src0_sel:WORD_1
	v_cvt_pk_f32_fp8_e32 v[192:193], v55
	v_cvt_pk_bf16_f32 v188, v188, v189
	v_cvt_pk_bf16_f32 v189, v190, v191
	v_cvt_pk_bf16_f32 v190, v192, v193
	v_cvt_scalef32_pk_bf16_fp8 v191, v55, 1.0 op_sel:[1,0,0]
	s_nop 1
	v_mfma_f32_16x16x32_bf16 v[188:191], v[6:9], v[188:191], 0
	v_cvt_scalef32_pk_bf16_fp8 v54, v56, 1.0
	v_cvt_scalef32_pk_bf16_fp8 v55, v56, 1.0 op_sel:[1,0,0]
	v_cvt_scalef32_pk_bf16_fp8 v56, v57, 1.0
	v_cvt_scalef32_pk_bf16_fp8 v57, v57, 1.0 op_sel:[1,0,0]
	v_cvt_pk_f32_fp8_e32 v[192:193], v47
	s_nop 0
	v_mfma_f32_16x16x32_bf16 v[54:57], v[2:5], v[54:57], v[188:191]
	s_nop 2
	v_cvt_pk_f32_fp8_e32 v[188:189], v46
	v_cvt_pk_f32_fp8_sdwa v[190:191], v46 src0_sel:WORD_1
	v_cvt_pk_bf16_f32 v188, v188, v189
	v_cvt_pk_bf16_f32 v189, v190, v191
	v_cvt_pk_bf16_f32 v190, v192, v193
	v_cvt_scalef32_pk_bf16_fp8 v191, v47, 1.0 op_sel:[1,0,0]
	s_nop 1
	v_mfma_f32_16x16x32_bf16 v[54:57], v[14:17], v[188:191], v[54:57]
	v_cvt_pk_f32_fp8_e32 v[190:191], v49
	v_cvt_scalef32_pk_bf16_fp8 v46, v48, 1.0
	v_cvt_scalef32_pk_bf16_fp8 v49, v49, 1.0 op_sel:[1,0,0]
	v_cvt_scalef32_pk_bf16_fp8 v47, v48, 1.0 op_sel:[1,0,0]
	v_cvt_pk_bf16_f32 v48, v190, v191
	s_nop 1
	s_nop 0
	v_mfma_f32_16x16x32_bf16 v[46:49], v[10:13], v[46:49], v[54:57]
	s_nop 7
	ds_bpermute_b32 v188, v166, v46
	ds_bpermute_b32 v189, v166, v47
	ds_bpermute_b32 v190, v166, v48
	ds_bpermute_b32 v191, v166, v49
	s_waitcnt vmcnt(12)
	v_cvt_pk_f32_fp8_e32 v[46:47], v38
	v_cvt_pk_f32_fp8_sdwa v[48:49], v38 src0_sel:WORD_1
	v_cvt_pk_f32_fp8_e32 v[54:55], v39
	v_cvt_pk_bf16_f32 v46, v46, v47
	v_cvt_pk_bf16_f32 v47, v48, v49
	v_cvt_pk_bf16_f32 v48, v54, v55
	v_cvt_scalef32_pk_bf16_fp8 v49, v39, 1.0 op_sel:[1,0,0]
	s_nop 1
	v_mfma_f32_16x16x32_bf16 v[46:49], v[6:9], v[46:49], 0
	v_cvt_scalef32_pk_bf16_fp8 v38, v40, 1.0
	v_cvt_scalef32_pk_bf16_fp8 v39, v40, 1.0 op_sel:[1,0,0]
	v_cvt_scalef32_pk_bf16_fp8 v40, v41, 1.0
	v_cvt_scalef32_pk_bf16_fp8 v41, v41, 1.0 op_sel:[1,0,0]
	v_cvt_pk_f32_fp8_e32 v[54:55], v35
	s_nop 0
	v_mfma_f32_16x16x32_bf16 v[38:41], v[2:5], v[38:41], v[46:49]
	s_nop 2
	v_cvt_pk_f32_fp8_e32 v[46:47], v34
	v_cvt_pk_f32_fp8_sdwa v[48:49], v34 src0_sel:WORD_1
	v_cvt_pk_bf16_f32 v46, v46, v47
	v_cvt_pk_bf16_f32 v47, v48, v49
	v_cvt_pk_bf16_f32 v48, v54, v55
	v_cvt_scalef32_pk_bf16_fp8 v49, v35, 1.0 op_sel:[1,0,0]
	s_nop 1
	v_mfma_f32_16x16x32_bf16 v[38:41], v[14:17], v[46:49], v[38:41]
	v_cvt_pk_f32_fp8_e32 v[48:49], v37
	v_cvt_scalef32_pk_bf16_fp8 v34, v36, 1.0
	v_cvt_scalef32_pk_bf16_fp8 v37, v37, 1.0 op_sel:[1,0,0]
	v_cvt_scalef32_pk_bf16_fp8 v35, v36, 1.0 op_sel:[1,0,0]
	v_cvt_pk_bf16_f32 v36, v48, v49
	s_nop 1
	s_nop 0
	v_mfma_f32_16x16x32_bf16 v[34:37], v[10:13], v[34:37], v[38:41]
	s_nop 7
	ds_bpermute_b32 v192, v166, v34
	ds_bpermute_b32 v193, v166, v35
	ds_bpermute_b32 v194, v166, v36
	ds_bpermute_b32 v195, v166, v37
	s_waitcnt vmcnt(10)
	v_cvt_pk_f32_fp8_e32 v[34:35], v30
	v_cvt_pk_f32_fp8_sdwa v[36:37], v30 src0_sel:WORD_1
	v_cvt_pk_f32_fp8_e32 v[38:39], v31
	v_cvt_pk_bf16_f32 v34, v34, v35
	v_cvt_pk_bf16_f32 v35, v36, v37
	v_cvt_pk_bf16_f32 v36, v38, v39
	v_cvt_scalef32_pk_bf16_fp8 v37, v31, 1.0 op_sel:[1,0,0]
	s_nop 1
	v_mfma_f32_16x16x32_bf16 v[34:37], v[6:9], v[34:37], 0
	v_cvt_scalef32_pk_bf16_fp8 v30, v32, 1.0
	v_cvt_scalef32_pk_bf16_fp8 v31, v32, 1.0 op_sel:[1,0,0]
	v_cvt_scalef32_pk_bf16_fp8 v32, v33, 1.0
	v_cvt_scalef32_pk_bf16_fp8 v33, v33, 1.0 op_sel:[1,0,0]
	v_cvt_pk_f32_fp8_e32 v[38:39], v27
	s_nop 0
	v_mfma_f32_16x16x32_bf16 v[30:33], v[2:5], v[30:33], v[34:37]
	s_nop 2
	v_cvt_pk_f32_fp8_e32 v[34:35], v26
	v_cvt_pk_f32_fp8_sdwa v[36:37], v26 src0_sel:WORD_1
	v_cvt_pk_bf16_f32 v34, v34, v35
	v_cvt_pk_bf16_f32 v35, v36, v37
	v_cvt_pk_bf16_f32 v36, v38, v39
	v_cvt_scalef32_pk_bf16_fp8 v37, v27, 1.0 op_sel:[1,0,0]
	s_nop 1
	v_mfma_f32_16x16x32_bf16 v[30:33], v[14:17], v[34:37], v[30:33]
	v_cvt_pk_f32_fp8_e32 v[36:37], v29
	v_cvt_scalef32_pk_bf16_fp8 v26, v28, 1.0
	v_cvt_scalef32_pk_bf16_fp8 v29, v29, 1.0 op_sel:[1,0,0]
	v_cvt_scalef32_pk_bf16_fp8 v27, v28, 1.0 op_sel:[1,0,0]
	v_cvt_pk_bf16_f32 v28, v36, v37
	s_nop 1
	s_nop 0
	v_mfma_f32_16x16x32_bf16 v[26:29], v[10:13], v[26:29], v[30:33]
	s_nop 7
	ds_bpermute_b32 v196, v166, v26
	ds_bpermute_b32 v197, v166, v27
	ds_bpermute_b32 v198, v166, v28
	ds_bpermute_b32 v199, v166, v29
	s_waitcnt vmcnt(8)
	v_cvt_pk_f32_fp8_e32 v[26:27], v22
	v_cvt_pk_f32_fp8_sdwa v[28:29], v22 src0_sel:WORD_1
	v_cvt_pk_f32_fp8_e32 v[30:31], v23
	v_cvt_pk_bf16_f32 v26, v26, v27
	v_cvt_pk_bf16_f32 v27, v28, v29
	v_cvt_pk_bf16_f32 v28, v30, v31
	v_cvt_scalef32_pk_bf16_fp8 v29, v23, 1.0 op_sel:[1,0,0]
	s_nop 1
	v_mfma_f32_16x16x32_bf16 v[26:29], v[6:9], v[26:29], 0
	v_cvt_scalef32_pk_bf16_fp8 v22, v24, 1.0
	v_cvt_scalef32_pk_bf16_fp8 v23, v24, 1.0 op_sel:[1,0,0]
	v_cvt_scalef32_pk_bf16_fp8 v24, v25, 1.0
	v_cvt_scalef32_pk_bf16_fp8 v25, v25, 1.0 op_sel:[1,0,0]
	v_cvt_pk_f32_fp8_e32 v[30:31], v19
	s_nop 0
	v_mfma_f32_16x16x32_bf16 v[22:25], v[2:5], v[22:25], v[26:29]
	s_nop 2
	v_cvt_pk_f32_fp8_e32 v[26:27], v18
	v_cvt_pk_f32_fp8_sdwa v[28:29], v18 src0_sel:WORD_1
	v_cvt_pk_bf16_f32 v26, v26, v27
	v_cvt_pk_bf16_f32 v27, v28, v29
	v_cvt_pk_bf16_f32 v28, v30, v31
	v_cvt_scalef32_pk_bf16_fp8 v29, v19, 1.0 op_sel:[1,0,0]
	s_nop 1
	v_mfma_f32_16x16x32_bf16 v[22:25], v[14:17], v[26:29], v[22:25]
	v_cvt_pk_f32_fp8_e32 v[28:29], v21
	v_cvt_scalef32_pk_bf16_fp8 v18, v20, 1.0
	v_cvt_scalef32_pk_bf16_fp8 v21, v21, 1.0 op_sel:[1,0,0]
	v_cvt_scalef32_pk_bf16_fp8 v19, v20, 1.0 op_sel:[1,0,0]
	v_cvt_pk_bf16_f32 v20, v28, v29
	s_nop 1
	s_nop 0
	v_mfma_f32_16x16x32_bf16 v[18:21], v[10:13], v[18:21], v[22:25]
	s_nop 7
	ds_bpermute_b32 v200, v166, v18
	ds_bpermute_b32 v201, v166, v19
	ds_bpermute_b32 v202, v166, v20
	ds_bpermute_b32 v203, v166, v21
	v_cmp_ge_u32_e32 vcc, s20, v151
	v_mov_b64_e32 v[18:19], 0
	v_mov_b64_e32 v[20:21], 0
	s_and_saveexec_b64 s[2:3], vcc
	s_cbranch_execz .LBB0_1222
	ds_read_u16 v20, v143 offset:33024
	s_waitcnt lgkmcnt(0)
	v_lshlrev_b32_e32 v86, 9, v20
	v_mov_b64_e32 v[20:21], v[86:87]

.LBB0_1228:
	s_or_b64 exec, exec, s[2:3]
	v_lshl_add_u64 v[26:27], v[116:117], 0, v[18:19]
	global_load_dwordx4 v[18:21], v[26:27], off offset:16
	s_nop 0
	global_load_dwordx4 v[26:29], v[26:27], off
	s_waitcnt vmcnt(14)
	v_cvt_pk_f32_fp8_e32 v[204:205], v78
	v_cvt_pk_f32_fp8_sdwa v[206:207], v78 src0_sel:WORD_1
	v_cvt_pk_f32_fp8_e32 v[208:209], v79
	v_cvt_pk_bf16_f32 v204, v204, v205
	v_cvt_pk_bf16_f32 v205, v206, v207
	v_cvt_pk_bf16_f32 v206, v208, v209
	v_cvt_scalef32_pk_bf16_fp8 v207, v79, 1.0 op_sel:[1,0,0]
	s_nop 1
	v_mfma_f32_16x16x32_bf16 v[204:207], v[6:9], v[204:207], 0
	v_cvt_scalef32_pk_bf16_fp8 v78, v80, 1.0
	v_cvt_scalef32_pk_bf16_fp8 v79, v80, 1.0 op_sel:[1,0,0]
	v_cvt_scalef32_pk_bf16_fp8 v80, v81, 1.0
	v_cvt_scalef32_pk_bf16_fp8 v81, v81, 1.0 op_sel:[1,0,0]
	v_cvt_pk_f32_fp8_e32 v[208:209], v75
	s_nop 0
	v_mfma_f32_16x16x32_bf16 v[78:81], v[2:5], v[78:81], v[204:207]
	s_nop 2
	v_cvt_pk_f32_fp8_e32 v[204:205], v74
	v_cvt_pk_f32_fp8_sdwa v[206:207], v74 src0_sel:WORD_1
	v_cvt_pk_bf16_f32 v204, v204, v205
	v_cvt_pk_bf16_f32 v205, v206, v207
	v_cvt_pk_bf16_f32 v206, v208, v209
	v_cvt_scalef32_pk_bf16_fp8 v207, v75, 1.0 op_sel:[1,0,0]
	s_nop 1
	v_mfma_f32_16x16x32_bf16 v[78:81], v[14:17], v[204:207], v[78:81]
	v_cvt_pk_f32_fp8_e32 v[206:207], v77
	v_cvt_scalef32_pk_bf16_fp8 v74, v76, 1.0
	v_cvt_scalef32_pk_bf16_fp8 v77, v77, 1.0 op_sel:[1,0,0]
	v_cvt_scalef32_pk_bf16_fp8 v75, v76, 1.0 op_sel:[1,0,0]
	v_cvt_pk_bf16_f32 v76, v206, v207
	s_nop 1
	s_nop 0
	v_mfma_f32_16x16x32_bf16 v[74:77], v[10:13], v[74:77], v[78:81]
	s_nop 7
	ds_bpermute_b32 v204, v166, v74
	ds_bpermute_b32 v205, v166, v75
	ds_bpermute_b32 v206, v166, v76
	ds_bpermute_b32 v207, v166, v77
	s_waitcnt vmcnt(12)
	v_cvt_pk_f32_fp8_e32 v[74:75], v70
	v_cvt_pk_f32_fp8_sdwa v[76:77], v70 src0_sel:WORD_1
	v_cvt_pk_f32_fp8_e32 v[78:79], v71
	v_cvt_pk_bf16_f32 v74, v74, v75
	v_cvt_pk_bf16_f32 v75, v76, v77
	v_cvt_pk_bf16_f32 v76, v78, v79
	v_cvt_scalef32_pk_bf16_fp8 v77, v71, 1.0 op_sel:[1,0,0]
	s_nop 1
	v_mfma_f32_16x16x32_bf16 v[74:77], v[6:9], v[74:77], 0
	v_cvt_scalef32_pk_bf16_fp8 v70, v72, 1.0
	v_cvt_scalef32_pk_bf16_fp8 v71, v72, 1.0 op_sel:[1,0,0]
	v_cvt_scalef32_pk_bf16_fp8 v72, v73, 1.0
	v_cvt_scalef32_pk_bf16_fp8 v73, v73, 1.0 op_sel:[1,0,0]
	v_cvt_pk_f32_fp8_e32 v[78:79], v63
	s_nop 0
	v_mfma_f32_16x16x32_bf16 v[70:73], v[2:5], v[70:73], v[74:77]
	s_nop 2
	v_cvt_pk_f32_fp8_e32 v[74:75], v62
	v_cvt_pk_f32_fp8_sdwa v[76:77], v62 src0_sel:WORD_1
	v_cvt_pk_bf16_f32 v74, v74, v75
	v_cvt_pk_bf16_f32 v75, v76, v77
	v_cvt_pk_bf16_f32 v76, v78, v79
	v_cvt_scalef32_pk_bf16_fp8 v77, v63, 1.0 op_sel:[1,0,0]
	s_nop 1
	v_mfma_f32_16x16x32_bf16 v[70:73], v[14:17], v[74:77], v[70:73]
	v_cvt_pk_f32_fp8_e32 v[76:77], v65
	v_cvt_scalef32_pk_bf16_fp8 v62, v64, 1.0
	v_cvt_scalef32_pk_bf16_fp8 v65, v65, 1.0 op_sel:[1,0,0]
	v_cvt_scalef32_pk_bf16_fp8 v63, v64, 1.0 op_sel:[1,0,0]
	v_cvt_pk_bf16_f32 v64, v76, v77
	s_nop 1
	s_nop 0
	v_mfma_f32_16x16x32_bf16 v[62:65], v[10:13], v[62:65], v[70:73]
	s_nop 7
	ds_bpermute_b32 v208, v166, v62
	ds_bpermute_b32 v209, v166, v63
	ds_bpermute_b32 v210, v166, v64
	ds_bpermute_b32 v211, v166, v65
	s_waitcnt vmcnt(10)
	v_cvt_pk_f32_fp8_e32 v[62:63], v58
	v_cvt_pk_f32_fp8_sdwa v[64:65], v58 src0_sel:WORD_1
	v_cvt_pk_f32_fp8_e32 v[70:71], v59
	v_cvt_pk_bf16_f32 v62, v62, v63
	v_cvt_pk_bf16_f32 v63, v64, v65
	v_cvt_pk_bf16_f32 v64, v70, v71
	v_cvt_scalef32_pk_bf16_fp8 v65, v59, 1.0 op_sel:[1,0,0]
	s_nop 1
	v_mfma_f32_16x16x32_bf16 v[62:65], v[6:9], v[62:65], 0
	v_cvt_scalef32_pk_bf16_fp8 v58, v60, 1.0
	v_cvt_scalef32_pk_bf16_fp8 v59, v60, 1.0 op_sel:[1,0,0]
	v_cvt_scalef32_pk_bf16_fp8 v60, v61, 1.0
	v_cvt_scalef32_pk_bf16_fp8 v61, v61, 1.0 op_sel:[1,0,0]
	v_cvt_pk_f32_fp8_e32 v[70:71], v43
	s_nop 0
	v_mfma_f32_16x16x32_bf16 v[58:61], v[2:5], v[58:61], v[62:65]
	s_nop 2
	v_cvt_pk_f32_fp8_e32 v[62:63], v42
	v_cvt_pk_f32_fp8_sdwa v[64:65], v42 src0_sel:WORD_1
	v_cvt_pk_bf16_f32 v62, v62, v63
	v_cvt_pk_bf16_f32 v63, v64, v65
	v_cvt_pk_bf16_f32 v64, v70, v71
	v_cvt_scalef32_pk_bf16_fp8 v65, v43, 1.0 op_sel:[1,0,0]
	s_nop 1
	v_mfma_f32_16x16x32_bf16 v[58:61], v[14:17], v[62:65], v[58:61]
	v_cvt_pk_f32_fp8_e32 v[64:65], v45
	v_cvt_scalef32_pk_bf16_fp8 v42, v44, 1.0
	v_cvt_scalef32_pk_bf16_fp8 v45, v45, 1.0 op_sel:[1,0,0]
	v_cvt_scalef32_pk_bf16_fp8 v43, v44, 1.0 op_sel:[1,0,0]
	v_cvt_pk_bf16_f32 v44, v64, v65
	s_nop 1
	s_nop 0
	v_mfma_f32_16x16x32_bf16 v[42:45], v[10:13], v[42:45], v[58:61]
	s_nop 7
	ds_bpermute_b32 v212, v166, v42
	ds_bpermute_b32 v213, v166, v43
	ds_bpermute_b32 v214, v166, v44
	ds_bpermute_b32 v215, v166, v45
	s_waitcnt vmcnt(8)
	v_cvt_scalef32_pk_bf16_fp8 v42, v66, 1.0
	v_cvt_scalef32_pk_bf16_fp8 v43, v66, 1.0 op_sel:[1,0,0]
	v_cvt_scalef32_pk_bf16_fp8 v44, v67, 1.0
	v_cvt_scalef32_pk_bf16_fp8 v45, v67, 1.0 op_sel:[1,0,0]
	s_nop 1
	v_mfma_f32_16x16x32_bf16 v[42:45], v[6:9], v[42:45], 0
	v_cvt_scalef32_pk_bf16_fp8 v58, v68, 1.0
	v_cvt_scalef32_pk_bf16_fp8 v59, v68, 1.0 op_sel:[1,0,0]
	v_cvt_scalef32_pk_bf16_fp8 v60, v69, 1.0
	v_cvt_scalef32_pk_bf16_fp8 v61, v69, 1.0 op_sel:[1,0,0]
	v_cvt_pk_f32_fp8_e32 v[62:63], v51
	s_nop 0
	v_mfma_f32_16x16x32_bf16 v[42:45], v[2:5], v[58:61], v[42:45]
	v_cvt_pk_f32_fp8_e32 v[58:59], v50
	v_cvt_pk_f32_fp8_sdwa v[60:61], v50 src0_sel:WORD_1
	v_cvt_pk_bf16_f32 v58, v58, v59
	v_cvt_pk_bf16_f32 v59, v60, v61
	v_cvt_pk_bf16_f32 v60, v62, v63
	v_cvt_scalef32_pk_bf16_fp8 v61, v51, 1.0 op_sel:[1,0,0]
	s_nop 1
	v_mfma_f32_16x16x32_bf16 v[42:45], v[14:17], v[58:61], v[42:45]
	v_cvt_pk_f32_fp8_e32 v[60:61], v53
	v_cvt_scalef32_pk_bf16_fp8 v50, v52, 1.0
	v_cvt_scalef32_pk_bf16_fp8 v53, v53, 1.0 op_sel:[1,0,0]
	v_cvt_scalef32_pk_bf16_fp8 v51, v52, 1.0 op_sel:[1,0,0]
	v_cvt_pk_bf16_f32 v52, v60, v61
	s_nop 1
	s_nop 0
	v_mfma_f32_16x16x32_bf16 v[42:45], v[10:13], v[50:53], v[42:45]
	s_nop 7
	ds_bpermute_b32 v216, v166, v42
	ds_bpermute_b32 v217, v166, v43
	ds_bpermute_b32 v218, v166, v44
	ds_bpermute_b32 v219, v166, v45
	v_cmp_ge_u32_e32 vcc, s20, v155
	v_mov_b64_e32 v[42:43], 0
	v_mov_b64_e32 v[44:45], 0
	s_and_saveexec_b64 s[2:3], vcc
	s_cbranch_execz .LBB0_1230
	ds_read_u16 v44, v143 offset:33152
	s_waitcnt lgkmcnt(0)
	v_lshlrev_b32_e32 v86, 9, v44
	v_mov_b64_e32 v[44:45], v[86:87]

.LBB0_1236:
	s_or_b64 exec, exec, s[2:3]
	v_lshl_add_u64 v[70:71], v[116:117], 0, v[62:63]
	global_load_dwordx4 v[62:65], v[70:71], off offset:16
	s_nop 0
	global_load_dwordx4 v[70:73], v[70:71], off
	s_waitcnt lgkmcnt(14)
	v_cndmask_b32_e64 v86, v184, v204, s[6:7]
	v_cndmask_b32_e64 v184, v185, v205, s[6:7]
	s_waitcnt lgkmcnt(11)
	v_cndmask_b32_e64 v86, v86, v208, s[8:9]
	s_waitcnt lgkmcnt(10)
	v_cndmask_b32_e64 v184, v184, v209, s[8:9]
	s_waitcnt lgkmcnt(7)
	v_cndmask_b32_e64 v86, v86, v212, s[10:11]
	v_cndmask_b32_e64 v185, v186, v206, s[6:7]
	v_cndmask_b32_e64 v186, v187, v207, s[6:7]
	s_waitcnt lgkmcnt(6)
	v_cndmask_b32_e64 v187, v184, v213, s[10:11]
	s_waitcnt lgkmcnt(3)
	v_cndmask_b32_e64 v184, v86, v216, s[12:13]
	v_cndmask_b32_e64 v86, v179, v188, s[6:7]
	v_cndmask_b32_e64 v179, v180, v189, s[6:7]
	v_cndmask_b32_e64 v180, v181, v190, s[6:7]
	v_cndmask_b32_e64 v181, v182, v191, s[6:7]
	v_cndmask_b32_e64 v185, v185, v210, s[8:9]
	v_cndmask_b32_e64 v186, v186, v211, s[8:9]
	v_cndmask_b32_e64 v86, v86, v192, s[8:9]
	v_cndmask_b32_e64 v179, v179, v193, s[8:9]
	v_cndmask_b32_e64 v180, v180, v194, s[8:9]
	v_cndmask_b32_e64 v181, v181, v195, s[8:9]
	v_cndmask_b32_e64 v204, v185, v214, s[10:11]
	v_cndmask_b32_e64 v205, v186, v215, s[10:11]
	v_cndmask_b32_e64 v86, v86, v196, s[10:11]
	v_cndmask_b32_e64 v182, v179, v197, s[10:11]
	v_cndmask_b32_e64 v188, v180, v198, s[10:11]
	v_cndmask_b32_e64 v189, v181, v199, s[10:11]
	s_waitcnt lgkmcnt(2)
	v_cndmask_b32_e64 v185, v187, v217, s[12:13]
	s_waitcnt lgkmcnt(1)
	v_cndmask_b32_e64 v186, v204, v218, s[12:13]
	s_waitcnt lgkmcnt(0)
	v_cndmask_b32_e64 v187, v205, v219, s[12:13]
	v_cndmask_b32_e64 v179, v86, v200, s[12:13]
	v_cndmask_b32_e64 v180, v182, v201, s[12:13]
	v_cndmask_b32_e64 v181, v188, v202, s[12:13]
	v_cndmask_b32_e64 v182, v189, v203, s[12:13]
	s_waitcnt vmcnt(14)
	v_cvt_pk_f32_fp8_e32 v[188:189], v54
	v_cvt_pk_f32_fp8_sdwa v[190:191], v54 src0_sel:WORD_1
	v_cvt_pk_f32_fp8_e32 v[192:193], v55
	v_cvt_pk_bf16_f32 v188, v188, v189
	v_cvt_pk_bf16_f32 v189, v190, v191
	v_cvt_pk_bf16_f32 v190, v192, v193
	v_cvt_scalef32_pk_bf16_fp8 v191, v55, 1.0 op_sel:[1,0,0]
	s_nop 1
	v_mfma_f32_16x16x32_bf16 v[188:191], v[6:9], v[188:191], 0
	v_cvt_scalef32_pk_bf16_fp8 v54, v56, 1.0
	v_cvt_scalef32_pk_bf16_fp8 v55, v56, 1.0 op_sel:[1,0,0]
	v_cvt_scalef32_pk_bf16_fp8 v56, v57, 1.0
	v_cvt_scalef32_pk_bf16_fp8 v57, v57, 1.0 op_sel:[1,0,0]
	v_cvt_pk_f32_fp8_e32 v[192:193], v47
	s_mov_b32 s2, 0
	v_mfma_f32_16x16x32_bf16 v[54:57], v[2:5], v[54:57], v[188:191]
	s_nop 2
	v_cvt_pk_f32_fp8_e32 v[188:189], v46
	v_cvt_pk_f32_fp8_sdwa v[190:191], v46 src0_sel:WORD_1
	v_cvt_pk_bf16_f32 v188, v188, v189
	v_cvt_pk_bf16_f32 v189, v190, v191
	v_cvt_pk_bf16_f32 v190, v192, v193
	v_cvt_scalef32_pk_bf16_fp8 v191, v47, 1.0 op_sel:[1,0,0]
	s_nop 1
	v_mfma_f32_16x16x32_bf16 v[54:57], v[14:17], v[188:191], v[54:57]
	v_cvt_pk_f32_fp8_e32 v[190:191], v49
	v_cvt_scalef32_pk_bf16_fp8 v46, v48, 1.0
	v_cvt_scalef32_pk_bf16_fp8 v49, v49, 1.0 op_sel:[1,0,0]
	v_cvt_scalef32_pk_bf16_fp8 v47, v48, 1.0 op_sel:[1,0,0]
	v_cvt_pk_bf16_f32 v48, v190, v191
	s_nop 1
	s_nop 0
	v_mfma_f32_16x16x32_bf16 v[46:49], v[10:13], v[46:49], v[54:57]
	s_nop 7
	ds_bpermute_b32 v48, v166, v48
	ds_bpermute_b32 v49, v166, v49
	ds_bpermute_b32 v46, v166, v46
	ds_bpermute_b32 v47, v166, v47
	s_waitcnt lgkmcnt(3)
	v_cndmask_b32_e64 v178, v178, v48, s[6:7]
	s_waitcnt lgkmcnt(2)
	v_cndmask_b32_e64 v183, v183, v49, s[6:7]
	s_waitcnt lgkmcnt(1)
	v_cndmask_b32_e64 v86, v176, v46, s[6:7]
	s_waitcnt lgkmcnt(0)
	v_cndmask_b32_e64 v188, v177, v47, s[6:7]
	s_waitcnt vmcnt(12)
	v_cvt_pk_f32_fp8_e32 v[46:47], v38
	v_cvt_pk_f32_fp8_sdwa v[48:49], v38 src0_sel:WORD_1
	v_cvt_pk_f32_fp8_e32 v[54:55], v39
	v_cvt_pk_bf16_f32 v46, v46, v47
	v_cvt_pk_bf16_f32 v47, v48, v49
	v_cvt_pk_bf16_f32 v48, v54, v55
	v_cvt_scalef32_pk_bf16_fp8 v49, v39, 1.0 op_sel:[1,0,0]
	s_nop 1
	v_mfma_f32_16x16x32_bf16 v[46:49], v[6:9], v[46:49], 0
	v_cvt_scalef32_pk_bf16_fp8 v38, v40, 1.0
	v_cvt_scalef32_pk_bf16_fp8 v39, v40, 1.0 op_sel:[1,0,0]
	v_cvt_scalef32_pk_bf16_fp8 v40, v41, 1.0
	v_cvt_scalef32_pk_bf16_fp8 v41, v41, 1.0 op_sel:[1,0,0]
	v_cvt_pk_f32_fp8_e32 v[54:55], v35
	s_nop 0
	v_mfma_f32_16x16x32_bf16 v[38:41], v[2:5], v[38:41], v[46:49]
	s_nop 2
	v_cvt_pk_f32_fp8_e32 v[46:47], v34
	v_cvt_pk_f32_fp8_sdwa v[48:49], v34 src0_sel:WORD_1
	v_cvt_pk_bf16_f32 v46, v46, v47
	v_cvt_pk_bf16_f32 v47, v48, v49
	v_cvt_pk_bf16_f32 v48, v54, v55
	v_cvt_scalef32_pk_bf16_fp8 v49, v35, 1.0 op_sel:[1,0,0]
	s_nop 1
	v_mfma_f32_16x16x32_bf16 v[38:41], v[14:17], v[46:49], v[38:41]
	v_cvt_pk_f32_fp8_e32 v[48:49], v37
	v_cvt_scalef32_pk_bf16_fp8 v34, v36, 1.0
	v_cvt_scalef32_pk_bf16_fp8 v37, v37, 1.0 op_sel:[1,0,0]
	v_cvt_scalef32_pk_bf16_fp8 v35, v36, 1.0 op_sel:[1,0,0]
	v_cvt_pk_bf16_f32 v36, v48, v49
	s_nop 1
	s_nop 0
	v_mfma_f32_16x16x32_bf16 v[34:37], v[10:13], v[34:37], v[38:41]
	s_nop 7
	ds_bpermute_b32 v34, v166, v34
	ds_bpermute_b32 v35, v166, v35
	ds_bpermute_b32 v36, v166, v36
	ds_bpermute_b32 v37, v166, v37
	s_waitcnt lgkmcnt(3)
	v_cndmask_b32_e64 v48, v86, v34, s[8:9]
	s_waitcnt lgkmcnt(2)
	v_cndmask_b32_e64 v49, v188, v35, s[8:9]
	s_waitcnt lgkmcnt(1)
	v_cndmask_b32_e64 v54, v178, v36, s[8:9]
	s_waitcnt lgkmcnt(0)
	v_cndmask_b32_e64 v55, v183, v37, s[8:9]
	s_waitcnt vmcnt(10)
	v_cvt_pk_f32_fp8_e32 v[34:35], v30
	v_cvt_pk_f32_fp8_sdwa v[36:37], v30 src0_sel:WORD_1
	v_cvt_pk_f32_fp8_e32 v[38:39], v31
	v_cvt_pk_bf16_f32 v34, v34, v35
	v_cvt_pk_bf16_f32 v35, v36, v37
	v_cvt_pk_bf16_f32 v36, v38, v39
	v_cvt_scalef32_pk_bf16_fp8 v37, v31, 1.0 op_sel:[1,0,0]
	s_nop 1
	v_mfma_f32_16x16x32_bf16 v[34:37], v[6:9], v[34:37], 0
	v_cvt_scalef32_pk_bf16_fp8 v30, v32, 1.0
	v_cvt_scalef32_pk_bf16_fp8 v31, v32, 1.0 op_sel:[1,0,0]
	v_cvt_scalef32_pk_bf16_fp8 v32, v33, 1.0
	v_cvt_scalef32_pk_bf16_fp8 v33, v33, 1.0 op_sel:[1,0,0]
	v_cvt_pk_f32_fp8_e32 v[38:39], v23
	s_nop 0
	v_mfma_f32_16x16x32_bf16 v[30:33], v[2:5], v[30:33], v[34:37]
	s_nop 2
	v_cvt_pk_f32_fp8_e32 v[34:35], v22
	v_cvt_pk_f32_fp8_sdwa v[36:37], v22 src0_sel:WORD_1
	v_cvt_pk_bf16_f32 v34, v34, v35
	v_cvt_pk_bf16_f32 v35, v36, v37
	v_cvt_pk_bf16_f32 v36, v38, v39
	v_cvt_scalef32_pk_bf16_fp8 v37, v23, 1.0 op_sel:[1,0,0]
	s_nop 1
	v_mfma_f32_16x16x32_bf16 v[30:33], v[14:17], v[34:37], v[30:33]
	v_cvt_pk_f32_fp8_e32 v[36:37], v25
	v_cvt_scalef32_pk_bf16_fp8 v22, v24, 1.0
	v_cvt_scalef32_pk_bf16_fp8 v25, v25, 1.0 op_sel:[1,0,0]
	v_cvt_scalef32_pk_bf16_fp8 v23, v24, 1.0 op_sel:[1,0,0]
	v_cvt_pk_bf16_f32 v24, v36, v37
	s_nop 1
	s_nop 0
	v_mfma_f32_16x16x32_bf16 v[22:25], v[10:13], v[22:25], v[30:33]
	s_nop 7
	ds_bpermute_b32 v22, v166, v22
	ds_bpermute_b32 v23, v166, v23
	ds_bpermute_b32 v24, v166, v24
	ds_bpermute_b32 v25, v166, v25
	s_waitcnt lgkmcnt(3)
	v_cndmask_b32_e64 v36, v48, v22, s[10:11]
	s_waitcnt lgkmcnt(2)
	v_cndmask_b32_e64 v37, v49, v23, s[10:11]
	s_waitcnt lgkmcnt(1)
	v_cndmask_b32_e64 v38, v54, v24, s[10:11]
	s_waitcnt lgkmcnt(0)
	v_cndmask_b32_e64 v39, v55, v25, s[10:11]
	s_waitcnt vmcnt(8)
	v_cvt_pk_f32_fp8_e32 v[22:23], v26
	v_cvt_pk_f32_fp8_sdwa v[24:25], v26 src0_sel:WORD_1
	v_cvt_pk_f32_fp8_e32 v[30:31], v27
	v_cvt_pk_bf16_f32 v22, v22, v23
	v_cvt_pk_bf16_f32 v23, v24, v25
	v_cvt_pk_bf16_f32 v24, v30, v31
	v_cvt_scalef32_pk_bf16_fp8 v25, v27, 1.0 op_sel:[1,0,0]
	s_nop 1
	v_mfma_f32_16x16x32_bf16 v[22:25], v[6:9], v[22:25], 0
	v_cvt_scalef32_pk_bf16_fp8 v26, v28, 1.0
	v_cvt_scalef32_pk_bf16_fp8 v27, v28, 1.0 op_sel:[1,0,0]
	v_cvt_scalef32_pk_bf16_fp8 v28, v29, 1.0
	v_cvt_scalef32_pk_bf16_fp8 v29, v29, 1.0 op_sel:[1,0,0]
	v_cvt_pk_f32_fp8_e32 v[30:31], v19
	s_nop 0
	v_mfma_f32_16x16x32_bf16 v[22:25], v[2:5], v[26:29], v[22:25]
	v_cvt_pk_f32_fp8_e32 v[26:27], v18
	v_cvt_pk_f32_fp8_sdwa v[28:29], v18 src0_sel:WORD_1
	v_cvt_pk_bf16_f32 v26, v26, v27
	v_cvt_pk_bf16_f32 v27, v28, v29
	v_cvt_pk_bf16_f32 v28, v30, v31
	v_cvt_scalef32_pk_bf16_fp8 v29, v19, 1.0 op_sel:[1,0,0]
	s_nop 1
	v_mfma_f32_16x16x32_bf16 v[22:25], v[14:17], v[26:29], v[22:25]
	v_cvt_pk_f32_fp8_e32 v[28:29], v21
	v_cvt_scalef32_pk_bf16_fp8 v18, v20, 1.0
	v_cvt_scalef32_pk_bf16_fp8 v21, v21, 1.0 op_sel:[1,0,0]
	v_cvt_scalef32_pk_bf16_fp8 v19, v20, 1.0 op_sel:[1,0,0]
	v_cvt_pk_bf16_f32 v20, v28, v29
	s_nop 1
	s_nop 0
	v_mfma_f32_16x16x32_bf16 v[18:21], v[10:13], v[18:21], v[22:25]
	s_nop 7
	ds_bpermute_b32 v18, v166, v18
	ds_bpermute_b32 v19, v166, v19
	ds_bpermute_b32 v20, v166, v20
	ds_bpermute_b32 v21, v166, v21
	s_waitcnt lgkmcnt(3)
	v_cndmask_b32_e64 v36, v36, v18, s[12:13]
	s_waitcnt lgkmcnt(2)
	v_cndmask_b32_e64 v37, v37, v19, s[12:13]
	s_waitcnt lgkmcnt(1)
	v_cndmask_b32_e64 v38, v38, v20, s[12:13]
	s_waitcnt lgkmcnt(0)
	v_cndmask_b32_e64 v39, v39, v21, s[12:13]
	s_waitcnt vmcnt(6)
	v_cvt_scalef32_pk_bf16_fp8 v18, v78, 1.0
	v_cvt_scalef32_pk_bf16_fp8 v19, v78, 1.0 op_sel:[1,0,0]
	v_cvt_scalef32_pk_bf16_fp8 v20, v79, 1.0
	v_cvt_scalef32_pk_bf16_fp8 v21, v79, 1.0 op_sel:[1,0,0]
	s_nop 1
	v_mfma_f32_16x16x32_bf16 v[18:21], v[6:9], v[18:21], 0
	v_cvt_scalef32_pk_bf16_fp8 v22, v80, 1.0
	v_cvt_scalef32_pk_bf16_fp8 v23, v80, 1.0 op_sel:[1,0,0]
	v_cvt_scalef32_pk_bf16_fp8 v24, v81, 1.0
	v_cvt_scalef32_pk_bf16_fp8 v25, v81, 1.0 op_sel:[1,0,0]
	s_nop 1
	v_mfma_f32_16x16x32_bf16 v[18:21], v[2:5], v[22:25], v[18:21]
	v_cvt_scalef32_pk_bf16_fp8 v22, v74, 1.0
	v_cvt_scalef32_pk_bf16_fp8 v23, v74, 1.0 op_sel:[1,0,0]
	v_cvt_scalef32_pk_bf16_fp8 v24, v75, 1.0
	v_cvt_scalef32_pk_bf16_fp8 v25, v75, 1.0 op_sel:[1,0,0]
	s_nop 1
	v_mfma_f32_16x16x32_bf16 v[18:21], v[14:17], v[22:25], v[18:21]
	v_cvt_scalef32_pk_bf16_fp8 v22, v76, 1.0
	v_cvt_scalef32_pk_bf16_fp8 v23, v76, 1.0 op_sel:[1,0,0]
	v_cvt_scalef32_pk_bf16_fp8 v24, v77, 1.0
	v_cvt_scalef32_pk_bf16_fp8 v25, v77, 1.0 op_sel:[1,0,0]
	s_nop 1
	s_nop 0
	v_mfma_f32_16x16x32_bf16 v[18:21], v[10:13], v[22:25], v[18:21]
	s_nop 7
	ds_bpermute_b32 v18, v166, v18
	ds_bpermute_b32 v19, v166, v19
	ds_bpermute_b32 v20, v166, v20
	ds_bpermute_b32 v21, v166, v21
	s_waitcnt lgkmcnt(3)
	v_cndmask_b32_e64 v30, v165, v18, s[6:7]
	s_waitcnt lgkmcnt(2)
	v_cndmask_b32_e64 v31, v169, v19, s[6:7]
	s_waitcnt lgkmcnt(1)
	v_cndmask_b32_e64 v32, v174, v20, s[6:7]
	s_waitcnt lgkmcnt(0)
	v_cndmask_b32_e64 v33, v175, v21, s[6:7]
	s_waitcnt vmcnt(4)
	v_cvt_scalef32_pk_bf16_fp8 v18, v66, 1.0
	v_cvt_scalef32_pk_bf16_fp8 v19, v66, 1.0 op_sel:[1,0,0]
	v_cvt_scalef32_pk_bf16_fp8 v20, v67, 1.0
	v_cvt_scalef32_pk_bf16_fp8 v21, v67, 1.0 op_sel:[1,0,0]
	s_nop 1
	v_mfma_f32_16x16x32_bf16 v[18:21], v[6:9], v[18:21], 0
	v_cvt_scalef32_pk_bf16_fp8 v22, v68, 1.0
	v_cvt_scalef32_pk_bf16_fp8 v23, v68, 1.0 op_sel:[1,0,0]
	v_cvt_scalef32_pk_bf16_fp8 v24, v69, 1.0
	v_cvt_scalef32_pk_bf16_fp8 v25, v69, 1.0 op_sel:[1,0,0]
	s_nop 1
	v_mfma_f32_16x16x32_bf16 v[18:21], v[2:5], v[22:25], v[18:21]
	v_cvt_scalef32_pk_bf16_fp8 v22, v58, 1.0
	v_cvt_scalef32_pk_bf16_fp8 v23, v58, 1.0 op_sel:[1,0,0]
	v_cvt_scalef32_pk_bf16_fp8 v24, v59, 1.0
	v_cvt_scalef32_pk_bf16_fp8 v25, v59, 1.0 op_sel:[1,0,0]
	s_nop 1
	v_mfma_f32_16x16x32_bf16 v[18:21], v[14:17], v[22:25], v[18:21]
	v_cvt_scalef32_pk_bf16_fp8 v22, v60, 1.0
	v_cvt_scalef32_pk_bf16_fp8 v23, v60, 1.0 op_sel:[1,0,0]
	v_cvt_scalef32_pk_bf16_fp8 v24, v61, 1.0
	v_cvt_scalef32_pk_bf16_fp8 v25, v61, 1.0 op_sel:[1,0,0]
	s_nop 1
	s_nop 0
	v_mfma_f32_16x16x32_bf16 v[18:21], v[10:13], v[22:25], v[18:21]
	s_nop 7
	ds_bpermute_b32 v18, v166, v18
	ds_bpermute_b32 v19, v166, v19
	ds_bpermute_b32 v20, v166, v20
	ds_bpermute_b32 v21, v166, v21
	s_waitcnt lgkmcnt(3)
	v_cndmask_b32_e64 v30, v30, v18, s[8:9]
	s_waitcnt lgkmcnt(2)
	v_cndmask_b32_e64 v31, v31, v19, s[8:9]
	s_waitcnt lgkmcnt(1)
	v_cndmask_b32_e64 v32, v32, v20, s[8:9]
	s_waitcnt lgkmcnt(0)
	v_cndmask_b32_e64 v33, v33, v21, s[8:9]
	s_waitcnt vmcnt(2)
	v_cvt_scalef32_pk_bf16_fp8 v18, v50, 1.0
	v_cvt_scalef32_pk_bf16_fp8 v19, v50, 1.0 op_sel:[1,0,0]
	v_cvt_scalef32_pk_bf16_fp8 v20, v51, 1.0
	v_cvt_scalef32_pk_bf16_fp8 v21, v51, 1.0 op_sel:[1,0,0]
	s_nop 1
	v_mfma_f32_16x16x32_bf16 v[18:21], v[6:9], v[18:21], 0
	v_cvt_scalef32_pk_bf16_fp8 v22, v52, 1.0
	v_cvt_scalef32_pk_bf16_fp8 v23, v52, 1.0 op_sel:[1,0,0]
	v_cvt_scalef32_pk_bf16_fp8 v24, v53, 1.0
	v_cvt_scalef32_pk_bf16_fp8 v25, v53, 1.0 op_sel:[1,0,0]
	s_nop 1
	v_mfma_f32_16x16x32_bf16 v[18:21], v[2:5], v[22:25], v[18:21]
	v_cvt_scalef32_pk_bf16_fp8 v22, v42, 1.0
	v_cvt_scalef32_pk_bf16_fp8 v23, v42, 1.0 op_sel:[1,0,0]
	v_cvt_scalef32_pk_bf16_fp8 v24, v43, 1.0
	v_cvt_scalef32_pk_bf16_fp8 v25, v43, 1.0 op_sel:[1,0,0]
	s_nop 1
	v_mfma_f32_16x16x32_bf16 v[18:21], v[14:17], v[22:25], v[18:21]
	v_cvt_scalef32_pk_bf16_fp8 v22, v44, 1.0
	v_cvt_scalef32_pk_bf16_fp8 v23, v44, 1.0 op_sel:[1,0,0]
	v_cvt_scalef32_pk_bf16_fp8 v24, v45, 1.0
	v_cvt_scalef32_pk_bf16_fp8 v25, v45, 1.0 op_sel:[1,0,0]
	s_nop 1
	s_nop 0
	v_mfma_f32_16x16x32_bf16 v[18:21], v[10:13], v[22:25], v[18:21]
	s_nop 7
	ds_bpermute_b32 v18, v166, v18
	ds_bpermute_b32 v19, v166, v19
	ds_bpermute_b32 v20, v166, v20
	ds_bpermute_b32 v21, v166, v21
	s_waitcnt lgkmcnt(3)
	v_cndmask_b32_e64 v26, v30, v18, s[10:11]
	s_waitcnt lgkmcnt(2)
	v_cndmask_b32_e64 v27, v31, v19, s[10:11]
	s_waitcnt lgkmcnt(1)
	v_cndmask_b32_e64 v28, v32, v20, s[10:11]
	s_waitcnt lgkmcnt(0)
	v_cndmask_b32_e64 v29, v33, v21, s[10:11]
	s_waitcnt vmcnt(0)
	v_cvt_scalef32_pk_bf16_fp8 v18, v70, 1.0
	v_cvt_scalef32_pk_bf16_fp8 v19, v70, 1.0 op_sel:[1,0,0]
	v_cvt_scalef32_pk_bf16_fp8 v20, v71, 1.0
	v_cvt_scalef32_pk_bf16_fp8 v21, v71, 1.0 op_sel:[1,0,0]
	s_nop 1
	v_mfma_f32_16x16x32_bf16 v[6:9], v[6:9], v[18:21], 0
	v_cvt_scalef32_pk_bf16_fp8 v18, v72, 1.0
	v_cvt_scalef32_pk_bf16_fp8 v19, v72, 1.0 op_sel:[1,0,0]
	v_cvt_scalef32_pk_bf16_fp8 v20, v73, 1.0
	v_cvt_scalef32_pk_bf16_fp8 v21, v73, 1.0 op_sel:[1,0,0]
	s_nop 1
	s_nop 0
	v_mfma_f32_16x16x32_bf16 v[2:5], v[2:5], v[18:21], v[6:9]
	s_nop 0
	v_cvt_scalef32_pk_bf16_fp8 v6, v62, 1.0
	v_cvt_scalef32_pk_bf16_fp8 v7, v62, 1.0 op_sel:[1,0,0]
	v_cvt_scalef32_pk_bf16_fp8 v8, v63, 1.0
	v_cvt_scalef32_pk_bf16_fp8 v9, v63, 1.0 op_sel:[1,0,0]
	s_nop 1
	s_nop 0
	v_mfma_f32_16x16x32_bf16 v[2:5], v[14:17], v[6:9], v[2:5]
	v_cvt_scalef32_pk_bf16_fp8 v6, v64, 1.0
	v_cvt_scalef32_pk_bf16_fp8 v7, v64, 1.0 op_sel:[1,0,0]
	v_cvt_scalef32_pk_bf16_fp8 v8, v65, 1.0
	v_cvt_scalef32_pk_bf16_fp8 v9, v65, 1.0 op_sel:[1,0,0]
	s_nop 1
	s_nop 0
	v_mfma_f32_16x16x32_bf16 v[2:5], v[10:13], v[6:9], v[2:5]
	s_nop 7
	ds_bpermute_b32 v2, v166, v2
	ds_bpermute_b32 v3, v166, v3
	ds_bpermute_b32 v4, v166, v4
	ds_bpermute_b32 v5, v166, v5
	s_waitcnt lgkmcnt(3)
	v_cndmask_b32_e64 v40, v26, v2, s[12:13]
	s_waitcnt lgkmcnt(2)
	v_cndmask_b32_e64 v41, v27, v3, s[12:13]
	s_waitcnt lgkmcnt(1)
	v_cndmask_b32_e64 v42, v28, v4, s[12:13]
	s_waitcnt lgkmcnt(0)
	v_cndmask_b32_e64 v43, v29, v5, s[12:13]
	ds_read_u16 v2, v142 offset:32768
	ds_read_u16 v4, v142 offset:32776
	ds_read_u16 v6, v142 offset:32784
	ds_read_u16 v8, v142 offset:32792
	ds_read_u16 v10, v142 offset:32800
	ds_read_u16 v12, v142 offset:32808
	ds_read_u16 v14, v142 offset:32816
	ds_read_u16 v16, v142 offset:32824
	s_waitcnt lgkmcnt(7)
	v_lshlrev_b32_e32 v86, 9, v2
	v_lshl_add_u64 v[2:3], v[118:119], 0, v[86:87]
	s_waitcnt lgkmcnt(6)
	v_lshlrev_b32_e32 v86, 9, v4
	v_lshl_add_u64 v[4:5], v[118:119], 0, v[86:87]
	s_waitcnt lgkmcnt(5)
	v_lshlrev_b32_e32 v86, 9, v6
	v_lshl_add_u64 v[6:7], v[118:119], 0, v[86:87]
	s_waitcnt lgkmcnt(4)
	v_lshlrev_b32_e32 v86, 9, v8
	v_lshl_add_u64 v[8:9], v[118:119], 0, v[86:87]
	s_waitcnt lgkmcnt(3)
	v_lshlrev_b32_e32 v86, 9, v10
	v_lshl_add_u64 v[10:11], v[118:119], 0, v[86:87]
	s_waitcnt lgkmcnt(2)
	v_lshlrev_b32_e32 v86, 9, v12
	v_lshl_add_u64 v[12:13], v[118:119], 0, v[86:87]
	s_waitcnt lgkmcnt(1)
	v_lshlrev_b32_e32 v86, 9, v14
	v_lshl_add_u64 v[14:15], v[118:119], 0, v[86:87]
	s_waitcnt lgkmcnt(0)
	v_lshlrev_b32_e32 v86, 9, v16
	v_lshl_add_u64 v[16:17], v[118:119], 0, v[86:87]
	global_load_dwordx2 v[2:3], v[2:3], off offset:128
	s_nop 0
	global_load_dwordx2 v[4:5], v[4:5], off offset:128
	s_nop 0
	global_load_dwordx2 v[6:7], v[6:7], off offset:128
	s_nop 0
	global_load_dwordx2 v[8:9], v[8:9], off offset:128
	s_nop 0
	global_load_dwordx2 v[10:11], v[10:11], off offset:128
	s_nop 0
	global_load_dwordx2 v[12:13], v[12:13], off offset:128
	s_nop 0
	global_load_dwordx2 v[14:15], v[14:15], off offset:128
	s_nop 0
	global_load_dwordx2 v[16:17], v[16:17], off offset:128
	ds_read_u16 v18, v142 offset:32832
	ds_read_u16 v20, v142 offset:32840
	ds_read_u16 v22, v142 offset:32848
	ds_read_u16 v24, v142 offset:32856
	ds_read_u16 v26, v142 offset:32864
	ds_read_u16 v28, v142 offset:32872
	ds_read_u16 v29, v142 offset:32880
	ds_read_u16 v34, v142 offset:32888
	s_waitcnt lgkmcnt(7)
	v_lshlrev_b32_e32 v86, 9, v18
	v_lshl_add_u64 v[18:19], v[118:119], 0, v[86:87]
	s_waitcnt lgkmcnt(6)
	v_lshlrev_b32_e32 v86, 9, v20
	v_lshl_add_u64 v[20:21], v[118:119], 0, v[86:87]
	s_waitcnt lgkmcnt(5)
	v_lshlrev_b32_e32 v86, 9, v22
	v_lshl_add_u64 v[22:23], v[118:119], 0, v[86:87]
	s_waitcnt lgkmcnt(4)
	v_lshlrev_b32_e32 v86, 9, v24
	v_lshl_add_u64 v[24:25], v[118:119], 0, v[86:87]
	s_waitcnt lgkmcnt(3)
	v_lshlrev_b32_e32 v86, 9, v26
	v_lshl_add_u64 v[26:27], v[118:119], 0, v[86:87]
	s_waitcnt lgkmcnt(2)
	v_lshlrev_b32_e32 v86, 9, v28
	v_lshl_add_u64 v[30:31], v[118:119], 0, v[86:87]
	s_waitcnt lgkmcnt(1)
	v_lshlrev_b32_e32 v86, 9, v29
	v_lshl_add_u64 v[32:33], v[118:119], 0, v[86:87]
	s_waitcnt lgkmcnt(0)
	v_lshlrev_b32_e32 v86, 9, v34
	v_lshl_add_u64 v[34:35], v[118:119], 0, v[86:87]
	global_load_dwordx2 v[18:19], v[18:19], off offset:128
	s_nop 0
	global_load_dwordx2 v[20:21], v[20:21], off offset:128
	s_nop 0
	global_load_dwordx2 v[22:23], v[22:23], off offset:128
	s_nop 0
	global_load_dwordx2 v[24:25], v[24:25], off offset:128
	s_nop 0
	global_load_dwordx2 v[28:29], v[26:27], off offset:128
	s_nop 0
	global_load_dwordx2 v[30:31], v[30:31], off offset:128
	s_nop 0
	global_load_dwordx2 v[32:33], v[32:33], off offset:128
	s_nop 0
	global_load_dwordx2 v[34:35], v[34:35], off offset:128
	s_add_i32 s3, s20, 4
	v_mul_f32_e32 v26, 0x3db504f3, v179
	v_cmp_lt_u32_e32 vcc, s14, v1
	v_mul_f32_e32 v27, 0x3db504f3, v36
	v_cmp_lt_u32_e64 s[14:15], s20, v160
	v_cndmask_b32_e32 v179, v26, v164, vcc
	v_mul_f32_e32 v26, 0x3db504f3, v180
	v_cndmask_b32_e32 v180, v26, v164, vcc
	v_mul_f32_e32 v26, 0x3db504f3, v181
	v_cndmask_b32_e32 v181, v26, v164, vcc
	v_mul_f32_e32 v26, 0x3db504f3, v182
	v_cndmask_b32_e64 v176, v27, v164, s[14:15]
	v_mul_f32_e32 v27, 0x3db504f3, v40
	v_cmp_lt_u32_e64 s[16:17], s20, v161
	v_cndmask_b32_e32 v182, v26, v164, vcc
	v_mul_f32_e32 v26, 0x3db504f3, v184
	v_cmp_lt_u32_e32 vcc, s20, v159
	v_cndmask_b32_e64 v165, v27, v164, s[16:17]
	v_max_f32_e32 v27, v176, v165
	v_cndmask_b32_e32 v184, v26, v164, vcc
	v_max3_f32 v27, v179, v184, v27
	ds_bpermute_b32 v36, v167, v27
	v_mul_f32_e32 v26, 0x3db504f3, v185
	v_cndmask_b32_e32 v185, v26, v164, vcc
	v_mul_f32_e32 v26, 0x3db504f3, v186
	v_cndmask_b32_e32 v186, v26, v164, vcc
	s_waitcnt lgkmcnt(0)
	v_max_f32_e32 v36, v36, v36
	v_max_f32_e32 v27, v27, v36
	ds_bpermute_b32 v36, v168, v27
	v_mul_f32_e32 v26, 0x3db504f3, v187
	v_cndmask_b32_e32 v187, v26, v164, vcc
	v_mul_f32_e32 v26, 0x3db504f3, v37
	v_mul_f32_e32 v37, 0x3db504f3, v41
	v_cndmask_b32_e64 v177, v26, v164, s[14:15]
	v_cndmask_b32_e64 v169, v37, v164, s[16:17]
	s_waitcnt lgkmcnt(0)
	v_max_f32_e32 v36, v36, v36
	v_max_f32_e32 v27, v27, v36
	v_max_f32_e32 v37, v177, v169
	ds_bpermute_b32 v36, v170, v27
	v_max3_f32 v37, v180, v185, v37
	v_mul_f32_e32 v26, 0x3db504f3, v38
	ds_bpermute_b32 v38, v167, v37
	v_cndmask_b32_e64 v178, v26, v164, s[14:15]
	v_mul_f32_e32 v26, 0x3db504f3, v39
	v_cndmask_b32_e64 v183, v26, v164, s[14:15]
	s_waitcnt lgkmcnt(1)
	v_max_f32_e32 v26, v36, v36
	v_max_f32_e32 v26, v27, v26
	s_waitcnt lgkmcnt(0)
	v_max_f32_e32 v36, v38, v38
	ds_bpermute_b32 v27, v171, v26
	v_max_f32_e32 v36, v37, v36
	ds_bpermute_b32 v37, v168, v36
	v_mul_f32_e32 v38, 0x3db504f3, v42
	v_cndmask_b32_e64 v174, v38, v164, s[16:17]
	s_waitcnt lgkmcnt(1)
	v_max_f32_e32 v27, v27, v27
	v_max_f32_e32 v26, v26, v27
	s_waitcnt lgkmcnt(0)
	v_max_f32_e32 v37, v37, v37
	ds_bpermute_b32 v27, v172, v26
	v_max_f32_e32 v36, v36, v37
	ds_bpermute_b32 v37, v170, v36
	v_mul_f32_e32 v38, 0x3db504f3, v43
	v_cndmask_b32_e64 v175, v38, v164, s[16:17]
	s_waitcnt lgkmcnt(1)
	v_max_f32_e32 v27, v27, v27
	v_max_f32_e32 v26, v26, v27
	s_waitcnt lgkmcnt(0)
	v_max_f32_e32 v37, v37, v37
	ds_bpermute_b32 v27, v173, v26
	v_max_f32_e32 v36, v36, v37
	ds_bpermute_b32 v37, v171, v36
	v_max_f32_e32 v39, v183, v175
	v_max3_f32 v39, v182, v187, v39
	s_waitcnt lgkmcnt(1)
	v_max_f32_e32 v27, v27, v27
	v_max_f32_e32 v26, v26, v27
	s_waitcnt lgkmcnt(0)
	v_max_f32_e32 v27, v37, v37
	v_max_f32_e32 v37, v178, v174
	v_max3_f32 v37, v181, v186, v37
	ds_bpermute_b32 v38, v167, v37
	ds_bpermute_b32 v40, v167, v39
	v_max_f32_e32 v27, v36, v27
	s_lshr_b32 s3, s3, 2
	s_mov_b32 s16, 32
	s_waitcnt lgkmcnt(1)
	v_max_f32_e32 v36, v38, v38
	v_max_f32_e32 v36, v37, v36
	s_waitcnt lgkmcnt(0)
	v_max_f32_e32 v38, v40, v40
	ds_bpermute_b32 v37, v168, v36
	v_max_f32_e32 v38, v39, v38
	ds_bpermute_b32 v39, v168, v38
	ds_bpermute_b32 v40, v172, v27
	v_mov_b32_e32 v74, v140
	s_waitcnt lgkmcnt(2)
	v_max_f32_e32 v37, v37, v37
	v_max_f32_e32 v36, v36, v37
	s_waitcnt lgkmcnt(1)
	v_max_f32_e32 v39, v39, v39
	ds_bpermute_b32 v37, v170, v36
	v_max_f32_e32 v38, v38, v39
	ds_bpermute_b32 v39, v170, v38
	s_waitcnt lgkmcnt(2)
	v_max_f32_e32 v40, v40, v40
	v_max_f32_e32 v27, v27, v40
	s_waitcnt lgkmcnt(1)
	v_max_f32_e32 v37, v37, v37
	v_max_f32_e32 v36, v36, v37
	s_waitcnt lgkmcnt(0)
	v_max_f32_e32 v39, v39, v39
	ds_bpermute_b32 v37, v171, v36
	v_max_f32_e32 v38, v38, v39
	ds_bpermute_b32 v39, v171, v38
	ds_bpermute_b32 v40, v173, v27
	s_waitcnt lgkmcnt(2)
	v_max_f32_e32 v37, v37, v37
	v_max_f32_e32 v36, v36, v37
	s_waitcnt lgkmcnt(1)
	v_max_f32_e32 v39, v39, v39
	ds_bpermute_b32 v37, v172, v36
	v_max_f32_e32 v38, v38, v39
	ds_bpermute_b32 v39, v172, v38
	s_waitcnt lgkmcnt(2)
	v_max_f32_e32 v40, v40, v40
	v_max_f32_e32 v27, v27, v40
	s_waitcnt lgkmcnt(1)
	v_max_f32_e32 v37, v37, v37
	v_max_f32_e32 v36, v36, v37
	s_waitcnt lgkmcnt(0)
	v_max_f32_e32 v39, v39, v39
	ds_bpermute_b32 v37, v173, v36
	v_max_f32_e32 v38, v38, v39
	ds_bpermute_b32 v39, v173, v38
	v_sub_f32_e32 v40, v184, v26
	v_mul_f32_e32 v40, 0x3fb8aa3b, v40
	s_waitcnt lgkmcnt(1)
	v_max_f32_e32 v37, v37, v37
	v_max_f32_e32 v44, v36, v37
	s_waitcnt lgkmcnt(0)
	v_max_f32_e32 v36, v39, v39
	v_max_f32_e32 v45, v38, v36
	v_sub_f32_e32 v36, v179, v26
	v_sub_f32_e32 v37, v180, v27
	v_sub_f32_e32 v38, v181, v44
	v_sub_f32_e32 v39, v182, v45
	v_mul_f32_e32 v36, 0x3fb8aa3b, v36
	v_mul_f32_e32 v37, 0x3fb8aa3b, v37
	v_mul_f32_e32 v38, 0x3fb8aa3b, v38
	v_mul_f32_e32 v39, 0x3fb8aa3b, v39
	v_exp_f32_e32 v36, v36
	v_exp_f32_e32 v37, v37
	v_exp_f32_e32 v38, v38
	v_exp_f32_e32 v39, v39
	v_exp_f32_e32 v40, v40
	v_add_f32_e32 v43, 0, v36
	v_sub_f32_e32 v41, v185, v27
	v_sub_f32_e32 v42, v186, v44
	ds_write_b128 v162, v[36:39]
	v_sub_f32_e32 v36, v187, v45
	v_mul_f32_e32 v41, 0x3fb8aa3b, v41
	v_mul_f32_e32 v42, 0x3fb8aa3b, v42
	v_mul_f32_e32 v36, 0x3fb8aa3b, v36
	v_add_f32_e32 v47, 0, v38
	v_exp_f32_e32 v41, v41
	v_exp_f32_e32 v42, v42
	v_add_f32_e32 v38, v40, v43
	v_exp_f32_e32 v43, v36
	v_sub_f32_e32 v36, v176, v26
	v_mul_f32_e32 v36, 0x3fb8aa3b, v36
	v_sub_f32_e32 v26, v165, v26
	v_exp_f32_e32 v36, v36
	v_mul_f32_e32 v26, 0x3fb8aa3b, v26
	ds_write_b128 v162, v[40:43] offset:1024
	v_exp_f32_e32 v40, v26
	v_add_f32_e32 v46, 0, v37
	v_sub_f32_e32 v26, v178, v44
	v_add_f32_e32 v48, 0, v39
	v_add_f32_e32 v39, v41, v46
	v_add_f32_e32 v41, v36, v38
	v_mul_f32_e32 v26, 0x3fb8aa3b, v26
	v_exp_f32_e32 v38, v26
	v_add_f32_e32 v26, v40, v41
	ds_bpermute_b32 v41, v167, v26
	v_add_f32_e32 v46, v42, v47
	v_add_f32_e32 v47, v43, v48
	v_sub_f32_e32 v37, v177, v27
	v_mul_f32_e32 v37, 0x3fb8aa3b, v37
	s_waitcnt lgkmcnt(0)
	v_add_f32_e32 v26, v26, v41
	ds_bpermute_b32 v43, v168, v26
	v_exp_f32_e32 v37, v37
	v_sub_f32_e32 v27, v169, v27
	v_mul_f32_e32 v27, 0x3fb8aa3b, v27
	v_exp_f32_e32 v41, v27
	s_waitcnt lgkmcnt(0)
	v_add_f32_e32 v26, v26, v43
	ds_bpermute_b32 v27, v170, v26
	v_add_f32_e32 v42, v37, v39
	v_sub_f32_e32 v39, v183, v45
	v_mul_f32_e32 v39, 0x3fb8aa3b, v39
	v_exp_f32_e32 v39, v39
	s_waitcnt lgkmcnt(0)
	v_add_f32_e32 v26, v26, v27
	ds_bpermute_b32 v27, v171, v26
	v_add_f32_e32 v46, v38, v46
	ds_write_b128 v162, v[36:39] offset:2048
	v_sub_f32_e32 v37, v174, v44
	v_mul_f32_e32 v37, 0x3fb8aa3b, v37
	v_add_f32_e32 v36, v41, v42
	v_exp_f32_e32 v42, v37
	v_sub_f32_e32 v37, v175, v45
	v_mul_f32_e32 v37, 0x3fb8aa3b, v37
	s_waitcnt lgkmcnt(1)
	v_add_f32_e32 v26, v26, v27
	v_exp_f32_e32 v43, v37
	ds_bpermute_b32 v27, v172, v26
	v_add_f32_e32 v47, v39, v47
	v_add_f32_e32 v37, v42, v46
	v_add_f32_e32 v38, v43, v47
	ds_bpermute_b32 v39, v167, v36
	s_waitcnt lgkmcnt(1)
	v_add_f32_e32 v66, v26, v27
	ds_bpermute_b32 v26, v167, v37
	ds_bpermute_b32 v27, v167, v38
	ds_bpermute_b32 v67, v173, v66
	s_waitcnt lgkmcnt(3)
	v_add_f32_e32 v36, v36, v39
	ds_bpermute_b32 v39, v168, v36
	s_waitcnt lgkmcnt(3)
	v_add_f32_e32 v26, v37, v26
	s_waitcnt lgkmcnt(2)
	v_add_f32_e32 v27, v38, v27
	ds_bpermute_b32 v37, v168, v26
	ds_bpermute_b32 v38, v168, v27
	s_waitcnt lgkmcnt(2)
	v_add_f32_e32 v36, v36, v39
	ds_bpermute_b32 v39, v170, v36
	ds_write_b128 v162, v[40:43] offset:3072
	s_waitcnt lgkmcnt(3)
	v_add_f32_e32 v26, v26, v37
	s_waitcnt lgkmcnt(2)
	v_add_f32_e32 v27, v27, v38
	ds_bpermute_b32 v37, v170, v26
	ds_bpermute_b32 v38, v170, v27
	s_waitcnt lgkmcnt(3)
	v_add_f32_e32 v36, v36, v39
	ds_bpermute_b32 v39, v171, v36
	s_waitcnt lgkmcnt(2)
	v_add_f32_e32 v26, v26, v37
	s_waitcnt lgkmcnt(1)
	v_add_f32_e32 v27, v27, v38
	ds_bpermute_b32 v37, v171, v26
	ds_bpermute_b32 v38, v171, v27
	s_waitcnt lgkmcnt(2)
	v_add_f32_e32 v36, v36, v39
	ds_bpermute_b32 v39, v172, v36
	s_waitcnt lgkmcnt(2)
	v_add_f32_e32 v26, v26, v37
	s_waitcnt lgkmcnt(1)
	v_add_f32_e32 v27, v27, v38
	ds_bpermute_b32 v37, v172, v26
	ds_bpermute_b32 v38, v172, v27
	s_waitcnt lgkmcnt(2)
	v_add_f32_e32 v68, v36, v39
	ds_bpermute_b32 v69, v173, v68
	s_waitcnt lgkmcnt(2)
	v_add_f32_e32 v70, v26, v37
	s_waitcnt lgkmcnt(1)
	v_add_f32_e32 v72, v27, v38
	ds_bpermute_b32 v71, v173, v70
	ds_bpermute_b32 v73, v173, v72
	v_mov_b32_e32 v27, 0
	v_mov_b32_e32 v26, v27
	v_mov_b32_e32 v37, v27
	v_mov_b32_e32 v36, v27
	v_mov_b32_e32 v39, v27
	v_mov_b32_e32 v38, v27
	v_mov_b32_e32 v41, v27
	v_mov_b32_e32 v40, v27
	v_mov_b32_e32 v43, v27
	v_mov_b32_e32 v42, v27
	v_mov_b32_e32 v45, v27
	v_mov_b32_e32 v44, v27
	v_mov_b32_e32 v47, v27
	v_mov_b32_e32 v46, v27
	v_mov_b32_e32 v49, v27
	v_mov_b32_e32 v48, v27
	v_mov_b32_e32 v51, v27
	v_mov_b32_e32 v50, v27
	v_mov_b32_e32 v53, v27
	v_mov_b32_e32 v52, v27
	v_mov_b32_e32 v55, v27
	v_mov_b32_e32 v54, v27
	v_mov_b32_e32 v57, v27
	v_mov_b32_e32 v56, v27
	v_mov_b32_e32 v59, v27
	v_mov_b32_e32 v58, v27
	v_mov_b32_e32 v61, v27
	v_mov_b32_e32 v60, v27
	v_mov_b32_e32 v63, v27
	v_mov_b32_e32 v62, v27
	v_mov_b32_e32 v65, v27
	v_mov_b32_e32 v64, v27
.LBB0_1237:
	s_add_i32 s17, s16, -16
	s_cmp_lt_u32 s17, s3
	v_add_u32_e32 v76, 64, v74
	s_cselect_b64 s[14:15], -1, 0
	s_cmp_ge_u32 s17, s3
	v_min_i32_e32 v77, 0xff, v76
	v_mov_b32_e32 v75, v74
	s_cbranch_scc1 .LBB0_1239
	v_lshl_add_u32 v237, v74, 1, v84
	ds_read_u16 v75, v237 offset:32896
	ds_read_u16 v100, v237 offset:32904
	ds_read_u16 v101, v237 offset:32912
	ds_read_u16 v102, v237 offset:32920
	ds_read_u16 v108, v237 offset:32928
	ds_read_u16 v109, v237 offset:32936
	ds_read_u16 v110, v237 offset:32944
	ds_read_u16 v111, v237 offset:32952
	s_waitcnt lgkmcnt(7)
	v_lshlrev_b32_e32 v86, 9, v75
	v_lshl_add_u64 v[78:79], v[118:119], 0, v[86:87]
	s_waitcnt lgkmcnt(6)
	v_lshlrev_b32_e32 v86, 9, v100
	v_lshl_add_u64 v[80:81], v[118:119], 0, v[86:87]
	s_waitcnt lgkmcnt(5)
	v_lshlrev_b32_e32 v86, 9, v101
	v_lshl_add_u64 v[98:99], v[118:119], 0, v[86:87]
	s_waitcnt lgkmcnt(4)
	v_lshlrev_b32_e32 v86, 9, v102
	v_lshl_add_u64 v[106:107], v[118:119], 0, v[86:87]
	s_waitcnt lgkmcnt(3)
	v_lshlrev_b32_e32 v86, 9, v108
	global_load_dwordx2 v[104:105], v[78:79], off offset:128
	global_load_dwordx2 v[102:103], v[80:81], off offset:128
	global_load_dwordx2 v[100:101], v[98:99], off offset:128
	s_nop 0
	global_load_dwordx2 v[98:99], v[106:107], off offset:128
	v_lshl_add_u64 v[78:79], v[118:119], 0, v[86:87]
	s_waitcnt lgkmcnt(2)
	v_lshlrev_b32_e32 v86, 9, v109
	v_lshl_add_u64 v[80:81], v[118:119], 0, v[86:87]
	s_waitcnt lgkmcnt(1)
	v_lshlrev_b32_e32 v86, 9, v110
	v_lshl_add_u64 v[106:107], v[118:119], 0, v[86:87]
	s_waitcnt lgkmcnt(0)
	v_lshlrev_b32_e32 v86, 9, v111
	v_lshl_add_u64 v[122:123], v[118:119], 0, v[86:87]
	global_load_dwordx2 v[112:113], v[78:79], off offset:128
	global_load_dwordx2 v[110:111], v[80:81], off offset:128
	global_load_dwordx2 v[108:109], v[106:107], off offset:128
	s_nop 0
	global_load_dwordx2 v[106:107], v[122:123], off offset:128
	ds_read_u16 v75, v237 offset:32960
	ds_read_u16 v124, v237 offset:32968
	ds_read_u16 v125, v237 offset:32976
	ds_read_u16 v126, v237 offset:32984
	ds_read_u16 v132, v237 offset:32992
	ds_read_u16 v133, v237 offset:33000
	ds_read_u16 v134, v237 offset:33008
	ds_read_u16 v135, v237 offset:33016
	s_waitcnt lgkmcnt(7)
	v_lshlrev_b32_e32 v86, 9, v75
	v_lshl_add_u64 v[78:79], v[118:119], 0, v[86:87]
	s_waitcnt lgkmcnt(6)
	v_lshlrev_b32_e32 v86, 9, v124
	v_lshl_add_u64 v[80:81], v[118:119], 0, v[86:87]
	s_waitcnt lgkmcnt(5)
	v_lshlrev_b32_e32 v86, 9, v125
	v_lshl_add_u64 v[122:123], v[118:119], 0, v[86:87]
	s_waitcnt lgkmcnt(4)
	v_lshlrev_b32_e32 v86, 9, v126
	v_lshl_add_u64 v[130:131], v[118:119], 0, v[86:87]
	s_waitcnt lgkmcnt(3)
	v_lshlrev_b32_e32 v86, 9, v132
	global_load_dwordx2 v[128:129], v[78:79], off offset:128
	global_load_dwordx2 v[126:127], v[80:81], off offset:128
	global_load_dwordx2 v[124:125], v[122:123], off offset:128
	s_nop 0
	global_load_dwordx2 v[122:123], v[130:131], off offset:128
	v_lshl_add_u64 v[78:79], v[118:119], 0, v[86:87]
	s_waitcnt lgkmcnt(2)
	v_lshlrev_b32_e32 v86, 9, v133
	v_lshl_add_u64 v[80:81], v[118:119], 0, v[86:87]
	s_waitcnt lgkmcnt(1)
	v_lshlrev_b32_e32 v86, 9, v134
	v_lshl_add_u64 v[130:131], v[118:119], 0, v[86:87]
	s_waitcnt lgkmcnt(0)
	v_lshlrev_b32_e32 v86, 9, v135
	v_lshl_add_u64 v[188:189], v[118:119], 0, v[86:87]
	global_load_dwordx2 v[136:137], v[78:79], off offset:128
	global_load_dwordx2 v[134:135], v[80:81], off offset:128
	global_load_dwordx2 v[132:133], v[130:131], off offset:128
	s_nop 0
	global_load_dwordx2 v[130:131], v[188:189], off offset:128
	v_lshl_or_b32 v75, s2, 2, v140
.LBB0_1239:
	v_lshl_add_u32 v236, v75, 4, v82
	ds_read_b128 v[220:223], v236
	ds_read_b128 v[224:227], v236 offset:64
	s_waitcnt vmcnt(15)
	v_cvt_pk_f32_fp8_e32 v[192:193], v3
	v_cvt_pk_f32_fp8_sdwa v[194:195], v3 src0_sel:WORD_1
	s_waitcnt lgkmcnt(1)
	v_cvt_pk_f32_fp8_e32 v[78:79], v2
	v_cvt_pk_f32_fp8_sdwa v[80:81], v2 src0_sel:WORD_1
	v_fmac_f32_e32 v40, v223, v78
	v_fmac_f32_e32 v41, v223, v79
	v_fmac_f32_e32 v38, v223, v80
	v_fmac_f32_e32 v39, v223, v81
	v_fmac_f32_e32 v36, v223, v192
	v_fmac_f32_e32 v37, v223, v193
	v_fmac_f32_e32 v26, v223, v194
	v_fmac_f32_e32 v27, v223, v195
	s_waitcnt lgkmcnt(0)
	v_fmac_f32_e32 v64, v220, v78
	v_fmac_f32_e32 v65, v220, v79
	v_fmac_f32_e32 v62, v220, v80
	v_fmac_f32_e32 v63, v220, v81
	v_fmac_f32_e32 v60, v220, v192
	v_fmac_f32_e32 v61, v220, v193
	v_fmac_f32_e32 v58, v220, v194
	v_fmac_f32_e32 v56, v221, v78
	v_fmac_f32_e32 v57, v221, v79
	v_fmac_f32_e32 v54, v221, v80
	v_fmac_f32_e32 v55, v221, v81
	v_fmac_f32_e32 v52, v221, v192
	v_fmac_f32_e32 v53, v221, v193
	v_fmac_f32_e32 v50, v221, v194
	v_fmac_f32_e32 v48, v222, v78
	v_fmac_f32_e32 v49, v222, v79
	v_fmac_f32_e32 v46, v222, v80
	v_fmac_f32_e32 v47, v222, v81
	v_fmac_f32_e32 v44, v222, v192
	v_fmac_f32_e32 v45, v222, v193
	v_fmac_f32_e32 v42, v222, v194
	s_waitcnt vmcnt(14)
	v_cvt_pk_f32_fp8_e32 v[78:79], v4
	v_cvt_pk_f32_fp8_sdwa v[80:81], v4 src0_sel:WORD_1
	v_cvt_pk_f32_fp8_e32 v[188:189], v5
	v_cvt_pk_f32_fp8_sdwa v[190:191], v5 src0_sel:WORD_1
	v_fmac_f32_e32 v40, v227, v78
	v_fmac_f32_e32 v41, v227, v79
	v_fmac_f32_e32 v38, v227, v80
	v_fmac_f32_e32 v39, v227, v81
	v_fmac_f32_e32 v36, v227, v188
	v_fmac_f32_e32 v37, v227, v189
	v_fmac_f32_e32 v26, v227, v190
	v_fmac_f32_e32 v27, v227, v191
	v_fmac_f32_e32 v64, v224, v78
	v_fmac_f32_e32 v56, v225, v78
	v_fmac_f32_e32 v48, v226, v78
	v_fmac_f32_e32 v60, v224, v188
	v_fmac_f32_e32 v52, v225, v188
	v_fmac_f32_e32 v44, v226, v188
	v_fmac_f32_e32 v59, v220, v195
	v_fmac_f32_e32 v51, v221, v195
	v_fmac_f32_e32 v43, v222, v195
	v_fmac_f32_e32 v65, v224, v79
	v_fmac_f32_e32 v62, v224, v80
	v_fmac_f32_e32 v63, v224, v81
	v_fmac_f32_e32 v57, v225, v79
	v_fmac_f32_e32 v54, v225, v80
	v_fmac_f32_e32 v55, v225, v81
	v_fmac_f32_e32 v49, v226, v79
	v_fmac_f32_e32 v46, v226, v80
	v_fmac_f32_e32 v47, v226, v81
	ds_read_b128 v[228:231], v236 offset:128
	v_fmac_f32_e32 v61, v224, v189
	v_fmac_f32_e32 v58, v224, v190
	v_fmac_f32_e32 v59, v224, v191
	v_fmac_f32_e32 v53, v225, v189
	v_fmac_f32_e32 v50, v225, v190
	v_fmac_f32_e32 v51, v225, v191
	v_fmac_f32_e32 v45, v226, v189
	v_fmac_f32_e32 v42, v226, v190
	v_fmac_f32_e32 v43, v226, v191
	ds_read_b128 v[232:235], v236 offset:192
	s_waitcnt vmcnt(13)
	v_cvt_pk_f32_fp8_e32 v[192:193], v7
	v_cvt_pk_f32_fp8_sdwa v[194:195], v7 src0_sel:WORD_1
	s_waitcnt lgkmcnt(1)
	v_cvt_pk_f32_fp8_e32 v[78:79], v6
	v_cvt_pk_f32_fp8_sdwa v[80:81], v6 src0_sel:WORD_1
	v_fmac_f32_e32 v64, v228, v78
	v_fmac_f32_e32 v65, v228, v79
	v_fmac_f32_e32 v62, v228, v80
	v_fmac_f32_e32 v63, v228, v81
	v_fmac_f32_e32 v60, v228, v192
	v_fmac_f32_e32 v61, v228, v193
	v_fmac_f32_e32 v58, v228, v194
	v_fmac_f32_e32 v59, v228, v195
	v_fmac_f32_e32 v56, v229, v78
	v_fmac_f32_e32 v57, v229, v79
	v_fmac_f32_e32 v54, v229, v80
	v_fmac_f32_e32 v55, v229, v81
	v_fmac_f32_e32 v52, v229, v192
	v_fmac_f32_e32 v53, v229, v193
	v_fmac_f32_e32 v50, v229, v194
	v_fmac_f32_e32 v51, v229, v195
	v_fmac_f32_e32 v48, v230, v78
	v_fmac_f32_e32 v49, v230, v79
	v_fmac_f32_e32 v46, v230, v80
	v_fmac_f32_e32 v47, v230, v81
	v_fmac_f32_e32 v44, v230, v192
	v_fmac_f32_e32 v45, v230, v193
	v_fmac_f32_e32 v42, v230, v194
	v_fmac_f32_e32 v43, v230, v195
	v_fmac_f32_e32 v40, v231, v78
	v_fmac_f32_e32 v41, v231, v79
	v_fmac_f32_e32 v38, v231, v80
	v_fmac_f32_e32 v39, v231, v81
	v_fmac_f32_e32 v36, v231, v192
	v_fmac_f32_e32 v37, v231, v193
	v_fmac_f32_e32 v26, v231, v194
	v_fmac_f32_e32 v27, v231, v195
	s_waitcnt vmcnt(12)
	v_cvt_pk_f32_fp8_e32 v[78:79], v8
	v_cvt_pk_f32_fp8_sdwa v[80:81], v8 src0_sel:WORD_1
	s_waitcnt lgkmcnt(0)
	v_cvt_pk_f32_fp8_e32 v[188:189], v9
	v_cvt_pk_f32_fp8_sdwa v[190:191], v9 src0_sel:WORD_1
	v_fmac_f32_e32 v64, v232, v78
	v_fmac_f32_e32 v65, v232, v79
	v_fmac_f32_e32 v62, v232, v80
	v_fmac_f32_e32 v63, v232, v81
	v_fmac_f32_e32 v60, v232, v188
	v_fmac_f32_e32 v61, v232, v189
	v_fmac_f32_e32 v58, v232, v190
	v_fmac_f32_e32 v59, v232, v191
	v_fmac_f32_e32 v56, v233, v78
	v_fmac_f32_e32 v57, v233, v79
	v_fmac_f32_e32 v54, v233, v80
	v_fmac_f32_e32 v55, v233, v81
	v_fmac_f32_e32 v52, v233, v188
	v_fmac_f32_e32 v53, v233, v189
	v_fmac_f32_e32 v50, v233, v190
	v_fmac_f32_e32 v51, v233, v191
	v_fmac_f32_e32 v48, v234, v78
	v_fmac_f32_e32 v49, v234, v79
	v_fmac_f32_e32 v46, v234, v80
	v_fmac_f32_e32 v47, v234, v81
	v_fmac_f32_e32 v44, v234, v188
	v_fmac_f32_e32 v45, v234, v189
	v_fmac_f32_e32 v42, v234, v190
	v_fmac_f32_e32 v43, v234, v191
	v_fmac_f32_e32 v40, v235, v78
	v_fmac_f32_e32 v41, v235, v79
	v_fmac_f32_e32 v38, v235, v80
	v_fmac_f32_e32 v39, v235, v81
	v_fmac_f32_e32 v36, v235, v188
	v_fmac_f32_e32 v37, v235, v189
	v_fmac_f32_e32 v26, v235, v190
	v_fmac_f32_e32 v27, v235, v191
	ds_read_b128 v[220:223], v236 offset:256
	ds_read_b128 v[224:227], v236 offset:320
	s_waitcnt vmcnt(11)
	v_cvt_pk_f32_fp8_e32 v[192:193], v11
	v_cvt_pk_f32_fp8_sdwa v[194:195], v11 src0_sel:WORD_1
	s_waitcnt lgkmcnt(1)
	v_cvt_pk_f32_fp8_e32 v[78:79], v10
	v_cvt_pk_f32_fp8_sdwa v[80:81], v10 src0_sel:WORD_1
	v_fmac_f32_e32 v40, v223, v78
	v_fmac_f32_e32 v41, v223, v79
	v_fmac_f32_e32 v38, v223, v80
	v_fmac_f32_e32 v39, v223, v81
	v_fmac_f32_e32 v36, v223, v192
	v_fmac_f32_e32 v37, v223, v193
	v_fmac_f32_e32 v26, v223, v194
	v_fmac_f32_e32 v27, v223, v195
	s_waitcnt lgkmcnt(0)
	v_fmac_f32_e32 v64, v220, v78
	v_fmac_f32_e32 v65, v220, v79
	v_fmac_f32_e32 v62, v220, v80
	v_fmac_f32_e32 v63, v220, v81
	v_fmac_f32_e32 v60, v220, v192
	v_fmac_f32_e32 v61, v220, v193
	v_fmac_f32_e32 v58, v220, v194
	v_fmac_f32_e32 v56, v221, v78
	v_fmac_f32_e32 v57, v221, v79
	v_fmac_f32_e32 v54, v221, v80
	v_fmac_f32_e32 v55, v221, v81
	v_fmac_f32_e32 v52, v221, v192
	v_fmac_f32_e32 v53, v221, v193
	v_fmac_f32_e32 v50, v221, v194
	v_fmac_f32_e32 v48, v222, v78
	v_fmac_f32_e32 v49, v222, v79
	v_fmac_f32_e32 v46, v222, v80
	v_fmac_f32_e32 v47, v222, v81
	v_fmac_f32_e32 v44, v222, v192
	v_fmac_f32_e32 v45, v222, v193
	v_fmac_f32_e32 v42, v222, v194
	s_waitcnt vmcnt(10)
	v_cvt_pk_f32_fp8_e32 v[78:79], v12
	v_cvt_pk_f32_fp8_sdwa v[80:81], v12 src0_sel:WORD_1
	v_cvt_pk_f32_fp8_e32 v[188:189], v13
	v_cvt_pk_f32_fp8_sdwa v[190:191], v13 src0_sel:WORD_1
	v_fmac_f32_e32 v40, v227, v78
	v_fmac_f32_e32 v41, v227, v79
	v_fmac_f32_e32 v38, v227, v80
	v_fmac_f32_e32 v39, v227, v81
	v_fmac_f32_e32 v36, v227, v188
	v_fmac_f32_e32 v37, v227, v189
	v_fmac_f32_e32 v26, v227, v190
	v_fmac_f32_e32 v27, v227, v191
	v_fmac_f32_e32 v64, v224, v78
	v_fmac_f32_e32 v56, v225, v78
	v_fmac_f32_e32 v48, v226, v78
	v_fmac_f32_e32 v60, v224, v188
	v_fmac_f32_e32 v52, v225, v188
	v_fmac_f32_e32 v44, v226, v188
	v_fmac_f32_e32 v59, v220, v195
	v_fmac_f32_e32 v51, v221, v195
	v_fmac_f32_e32 v43, v222, v195
	v_fmac_f32_e32 v65, v224, v79
	v_fmac_f32_e32 v62, v224, v80
	v_fmac_f32_e32 v63, v224, v81
	v_fmac_f32_e32 v57, v225, v79
	v_fmac_f32_e32 v54, v225, v80
	v_fmac_f32_e32 v55, v225, v81
	v_fmac_f32_e32 v49, v226, v79
	v_fmac_f32_e32 v46, v226, v80
	v_fmac_f32_e32 v47, v226, v81
	ds_read_b128 v[228:231], v236 offset:384
	v_fmac_f32_e32 v61, v224, v189
	v_fmac_f32_e32 v58, v224, v190
	v_fmac_f32_e32 v59, v224, v191
	v_fmac_f32_e32 v53, v225, v189
	v_fmac_f32_e32 v50, v225, v190
	v_fmac_f32_e32 v51, v225, v191
	v_fmac_f32_e32 v45, v226, v189
	v_fmac_f32_e32 v42, v226, v190
	v_fmac_f32_e32 v43, v226, v191
	ds_read_b128 v[232:235], v236 offset:448
	s_waitcnt vmcnt(9)
	v_cvt_pk_f32_fp8_e32 v[192:193], v15
	v_cvt_pk_f32_fp8_sdwa v[194:195], v15 src0_sel:WORD_1
	s_waitcnt lgkmcnt(1)
	v_cvt_pk_f32_fp8_e32 v[78:79], v14
	v_cvt_pk_f32_fp8_sdwa v[80:81], v14 src0_sel:WORD_1
	v_fmac_f32_e32 v64, v228, v78
	v_fmac_f32_e32 v65, v228, v79
	v_fmac_f32_e32 v62, v228, v80
	v_fmac_f32_e32 v63, v228, v81
	v_fmac_f32_e32 v60, v228, v192
	v_fmac_f32_e32 v61, v228, v193
	v_fmac_f32_e32 v58, v228, v194
	v_fmac_f32_e32 v59, v228, v195
	v_fmac_f32_e32 v56, v229, v78
	v_fmac_f32_e32 v57, v229, v79
	v_fmac_f32_e32 v54, v229, v80
	v_fmac_f32_e32 v55, v229, v81
	v_fmac_f32_e32 v52, v229, v192
	v_fmac_f32_e32 v53, v229, v193
	v_fmac_f32_e32 v50, v229, v194
	v_fmac_f32_e32 v51, v229, v195
	v_fmac_f32_e32 v48, v230, v78
	v_fmac_f32_e32 v49, v230, v79
	v_fmac_f32_e32 v46, v230, v80
	v_fmac_f32_e32 v47, v230, v81
	v_fmac_f32_e32 v44, v230, v192
	v_fmac_f32_e32 v45, v230, v193
	v_fmac_f32_e32 v42, v230, v194
	v_fmac_f32_e32 v43, v230, v195
	v_fmac_f32_e32 v40, v231, v78
	v_fmac_f32_e32 v41, v231, v79
	v_fmac_f32_e32 v38, v231, v80
	v_fmac_f32_e32 v39, v231, v81
	v_fmac_f32_e32 v36, v231, v192
	v_fmac_f32_e32 v37, v231, v193
	v_fmac_f32_e32 v26, v231, v194
	v_fmac_f32_e32 v27, v231, v195
	s_waitcnt vmcnt(8)
	v_cvt_pk_f32_fp8_e32 v[78:79], v16
	v_cvt_pk_f32_fp8_sdwa v[80:81], v16 src0_sel:WORD_1
	s_waitcnt lgkmcnt(0)
	v_cvt_pk_f32_fp8_e32 v[188:189], v17
	v_cvt_pk_f32_fp8_sdwa v[190:191], v17 src0_sel:WORD_1
	v_fmac_f32_e32 v64, v232, v78
	v_fmac_f32_e32 v65, v232, v79
	v_fmac_f32_e32 v62, v232, v80
	v_fmac_f32_e32 v63, v232, v81
	v_fmac_f32_e32 v60, v232, v188
	v_fmac_f32_e32 v61, v232, v189
	v_fmac_f32_e32 v58, v232, v190
	v_fmac_f32_e32 v59, v232, v191
	v_fmac_f32_e32 v56, v233, v78
	v_fmac_f32_e32 v57, v233, v79
	v_fmac_f32_e32 v54, v233, v80
	v_fmac_f32_e32 v55, v233, v81
	v_fmac_f32_e32 v52, v233, v188
	v_fmac_f32_e32 v53, v233, v189
	v_fmac_f32_e32 v50, v233, v190
	v_fmac_f32_e32 v51, v233, v191
	v_fmac_f32_e32 v48, v234, v78
	v_fmac_f32_e32 v49, v234, v79
	v_fmac_f32_e32 v46, v234, v80
	v_fmac_f32_e32 v47, v234, v81
	v_fmac_f32_e32 v44, v234, v188
	v_fmac_f32_e32 v45, v234, v189
	v_fmac_f32_e32 v42, v234, v190
	v_fmac_f32_e32 v43, v234, v191
	v_fmac_f32_e32 v40, v235, v78
	v_fmac_f32_e32 v41, v235, v79
	v_fmac_f32_e32 v38, v235, v80
	v_fmac_f32_e32 v39, v235, v81
	v_fmac_f32_e32 v36, v235, v188
	v_fmac_f32_e32 v37, v235, v189
	v_fmac_f32_e32 v26, v235, v190
	v_fmac_f32_e32 v27, v235, v191
	ds_read_b128 v[220:223], v236 offset:512
	ds_read_b128 v[224:227], v236 offset:576
	s_waitcnt vmcnt(7)
	v_cvt_pk_f32_fp8_e32 v[192:193], v19
	v_cvt_pk_f32_fp8_sdwa v[194:195], v19 src0_sel:WORD_1
	s_waitcnt lgkmcnt(1)
	v_cvt_pk_f32_fp8_e32 v[78:79], v18
	v_cvt_pk_f32_fp8_sdwa v[80:81], v18 src0_sel:WORD_1
	v_fmac_f32_e32 v40, v223, v78
	v_fmac_f32_e32 v41, v223, v79
	v_fmac_f32_e32 v38, v223, v80
	v_fmac_f32_e32 v39, v223, v81
	v_fmac_f32_e32 v36, v223, v192
	v_fmac_f32_e32 v37, v223, v193
	v_fmac_f32_e32 v26, v223, v194
	v_fmac_f32_e32 v27, v223, v195
	s_waitcnt lgkmcnt(0)
	v_fmac_f32_e32 v64, v220, v78
	v_fmac_f32_e32 v65, v220, v79
	v_fmac_f32_e32 v62, v220, v80
	v_fmac_f32_e32 v63, v220, v81
	v_fmac_f32_e32 v60, v220, v192
	v_fmac_f32_e32 v61, v220, v193
	v_fmac_f32_e32 v58, v220, v194
	v_fmac_f32_e32 v56, v221, v78
	v_fmac_f32_e32 v57, v221, v79
	v_fmac_f32_e32 v54, v221, v80
	v_fmac_f32_e32 v55, v221, v81
	v_fmac_f32_e32 v52, v221, v192
	v_fmac_f32_e32 v53, v221, v193
	v_fmac_f32_e32 v50, v221, v194
	v_fmac_f32_e32 v48, v222, v78
	v_fmac_f32_e32 v49, v222, v79
	v_fmac_f32_e32 v46, v222, v80
	v_fmac_f32_e32 v47, v222, v81
	v_fmac_f32_e32 v44, v222, v192
	v_fmac_f32_e32 v45, v222, v193
	v_fmac_f32_e32 v42, v222, v194
	s_waitcnt vmcnt(6)
	v_cvt_pk_f32_fp8_e32 v[78:79], v20
	v_cvt_pk_f32_fp8_sdwa v[80:81], v20 src0_sel:WORD_1
	v_cvt_pk_f32_fp8_e32 v[188:189], v21
	v_cvt_pk_f32_fp8_sdwa v[190:191], v21 src0_sel:WORD_1
	v_fmac_f32_e32 v40, v227, v78
	v_fmac_f32_e32 v41, v227, v79
	v_fmac_f32_e32 v38, v227, v80
	v_fmac_f32_e32 v39, v227, v81
	v_fmac_f32_e32 v36, v227, v188
	v_fmac_f32_e32 v37, v227, v189
	v_fmac_f32_e32 v26, v227, v190
	v_fmac_f32_e32 v27, v227, v191
	v_fmac_f32_e32 v64, v224, v78
	v_fmac_f32_e32 v56, v225, v78
	v_fmac_f32_e32 v48, v226, v78
	v_fmac_f32_e32 v60, v224, v188
	v_fmac_f32_e32 v52, v225, v188
	v_fmac_f32_e32 v44, v226, v188
	v_fmac_f32_e32 v59, v220, v195
	v_fmac_f32_e32 v51, v221, v195
	v_fmac_f32_e32 v43, v222, v195
	v_fmac_f32_e32 v65, v224, v79
	v_fmac_f32_e32 v62, v224, v80
	v_fmac_f32_e32 v63, v224, v81
	v_fmac_f32_e32 v57, v225, v79
	v_fmac_f32_e32 v54, v225, v80
	v_fmac_f32_e32 v55, v225, v81
	v_fmac_f32_e32 v49, v226, v79
	v_fmac_f32_e32 v46, v226, v80
	v_fmac_f32_e32 v47, v226, v81
	ds_read_b128 v[228:231], v236 offset:640
	v_fmac_f32_e32 v61, v224, v189
	v_fmac_f32_e32 v58, v224, v190
	v_fmac_f32_e32 v59, v224, v191
	v_fmac_f32_e32 v53, v225, v189
	v_fmac_f32_e32 v50, v225, v190
	v_fmac_f32_e32 v51, v225, v191
	v_fmac_f32_e32 v45, v226, v189
	v_fmac_f32_e32 v42, v226, v190
	v_fmac_f32_e32 v43, v226, v191
	ds_read_b128 v[232:235], v236 offset:704
	s_waitcnt vmcnt(5)
	v_cvt_pk_f32_fp8_e32 v[192:193], v23
	v_cvt_pk_f32_fp8_sdwa v[194:195], v23 src0_sel:WORD_1
	s_waitcnt lgkmcnt(1)
	v_cvt_pk_f32_fp8_e32 v[78:79], v22
	v_cvt_pk_f32_fp8_sdwa v[80:81], v22 src0_sel:WORD_1
	v_fmac_f32_e32 v64, v228, v78
	v_fmac_f32_e32 v65, v228, v79
	v_fmac_f32_e32 v62, v228, v80
	v_fmac_f32_e32 v63, v228, v81
	v_fmac_f32_e32 v60, v228, v192
	v_fmac_f32_e32 v61, v228, v193
	v_fmac_f32_e32 v58, v228, v194
	v_fmac_f32_e32 v59, v228, v195
	v_fmac_f32_e32 v56, v229, v78
	v_fmac_f32_e32 v57, v229, v79
	v_fmac_f32_e32 v54, v229, v80
	v_fmac_f32_e32 v55, v229, v81
	v_fmac_f32_e32 v52, v229, v192
	v_fmac_f32_e32 v53, v229, v193
	v_fmac_f32_e32 v50, v229, v194
	v_fmac_f32_e32 v51, v229, v195
	v_fmac_f32_e32 v48, v230, v78
	v_fmac_f32_e32 v49, v230, v79
	v_fmac_f32_e32 v46, v230, v80
	v_fmac_f32_e32 v47, v230, v81
	v_fmac_f32_e32 v44, v230, v192
	v_fmac_f32_e32 v45, v230, v193
	v_fmac_f32_e32 v42, v230, v194
	v_fmac_f32_e32 v43, v230, v195
	v_fmac_f32_e32 v40, v231, v78
	v_fmac_f32_e32 v41, v231, v79
	v_fmac_f32_e32 v38, v231, v80
	v_fmac_f32_e32 v39, v231, v81
	v_fmac_f32_e32 v36, v231, v192
	v_fmac_f32_e32 v37, v231, v193
	v_fmac_f32_e32 v26, v231, v194
	v_fmac_f32_e32 v27, v231, v195
	s_waitcnt vmcnt(4)
	v_cvt_pk_f32_fp8_e32 v[78:79], v24
	v_cvt_pk_f32_fp8_sdwa v[80:81], v24 src0_sel:WORD_1
	s_waitcnt lgkmcnt(0)
	v_cvt_pk_f32_fp8_e32 v[188:189], v25
	v_cvt_pk_f32_fp8_sdwa v[190:191], v25 src0_sel:WORD_1
	v_fmac_f32_e32 v64, v232, v78
	v_fmac_f32_e32 v65, v232, v79
	v_fmac_f32_e32 v62, v232, v80
	v_fmac_f32_e32 v63, v232, v81
	v_fmac_f32_e32 v60, v232, v188
	v_fmac_f32_e32 v61, v232, v189
	v_fmac_f32_e32 v58, v232, v190
	v_fmac_f32_e32 v59, v232, v191
	v_fmac_f32_e32 v56, v233, v78
	v_fmac_f32_e32 v57, v233, v79
	v_fmac_f32_e32 v54, v233, v80
	v_fmac_f32_e32 v55, v233, v81
	v_fmac_f32_e32 v52, v233, v188
	v_fmac_f32_e32 v53, v233, v189
	v_fmac_f32_e32 v50, v233, v190
	v_fmac_f32_e32 v51, v233, v191
	v_fmac_f32_e32 v48, v234, v78
	v_fmac_f32_e32 v49, v234, v79
	v_fmac_f32_e32 v46, v234, v80
	v_fmac_f32_e32 v47, v234, v81
	v_fmac_f32_e32 v44, v234, v188
	v_fmac_f32_e32 v45, v234, v189
	v_fmac_f32_e32 v42, v234, v190
	v_fmac_f32_e32 v43, v234, v191
	v_fmac_f32_e32 v40, v235, v78
	v_fmac_f32_e32 v41, v235, v79
	v_fmac_f32_e32 v38, v235, v80
	v_fmac_f32_e32 v39, v235, v81
	v_fmac_f32_e32 v36, v235, v188
	v_fmac_f32_e32 v37, v235, v189
	v_fmac_f32_e32 v26, v235, v190
	v_fmac_f32_e32 v27, v235, v191
	ds_read_b128 v[220:223], v236 offset:768
	ds_read_b128 v[224:227], v236 offset:832
	s_waitcnt vmcnt(3)
	v_cvt_pk_f32_fp8_e32 v[192:193], v29
	v_cvt_pk_f32_fp8_sdwa v[194:195], v29 src0_sel:WORD_1
	s_waitcnt lgkmcnt(1)
	v_cvt_pk_f32_fp8_e32 v[78:79], v28
	v_cvt_pk_f32_fp8_sdwa v[80:81], v28 src0_sel:WORD_1
	v_fmac_f32_e32 v40, v223, v78
	v_fmac_f32_e32 v41, v223, v79
	v_fmac_f32_e32 v38, v223, v80
	v_fmac_f32_e32 v39, v223, v81
	v_fmac_f32_e32 v36, v223, v192
	v_fmac_f32_e32 v37, v223, v193
	v_fmac_f32_e32 v26, v223, v194
	v_fmac_f32_e32 v27, v223, v195
	s_waitcnt lgkmcnt(0)
	v_fmac_f32_e32 v64, v220, v78
	v_fmac_f32_e32 v65, v220, v79
	v_fmac_f32_e32 v62, v220, v80
	v_fmac_f32_e32 v63, v220, v81
	v_fmac_f32_e32 v60, v220, v192
	v_fmac_f32_e32 v61, v220, v193
	v_fmac_f32_e32 v58, v220, v194
	v_fmac_f32_e32 v56, v221, v78
	v_fmac_f32_e32 v57, v221, v79
	v_fmac_f32_e32 v54, v221, v80
	v_fmac_f32_e32 v55, v221, v81
	v_fmac_f32_e32 v52, v221, v192
	v_fmac_f32_e32 v53, v221, v193
	v_fmac_f32_e32 v50, v221, v194
	v_fmac_f32_e32 v48, v222, v78
	v_fmac_f32_e32 v49, v222, v79
	v_fmac_f32_e32 v46, v222, v80
	v_fmac_f32_e32 v47, v222, v81
	v_fmac_f32_e32 v44, v222, v192
	v_fmac_f32_e32 v45, v222, v193
	v_fmac_f32_e32 v42, v222, v194
	s_waitcnt vmcnt(2)
	v_cvt_pk_f32_fp8_e32 v[78:79], v30
	v_cvt_pk_f32_fp8_sdwa v[80:81], v30 src0_sel:WORD_1
	v_cvt_pk_f32_fp8_e32 v[188:189], v31
	v_cvt_pk_f32_fp8_sdwa v[190:191], v31 src0_sel:WORD_1
	v_fmac_f32_e32 v40, v227, v78
	v_fmac_f32_e32 v41, v227, v79
	v_fmac_f32_e32 v38, v227, v80
	v_fmac_f32_e32 v39, v227, v81
	v_fmac_f32_e32 v36, v227, v188
	v_fmac_f32_e32 v37, v227, v189
	v_fmac_f32_e32 v26, v227, v190
	v_fmac_f32_e32 v27, v227, v191
	v_fmac_f32_e32 v64, v224, v78
	v_fmac_f32_e32 v56, v225, v78
	v_fmac_f32_e32 v48, v226, v78
	v_fmac_f32_e32 v60, v224, v188
	v_fmac_f32_e32 v52, v225, v188
	v_fmac_f32_e32 v44, v226, v188
	v_fmac_f32_e32 v59, v220, v195
	v_fmac_f32_e32 v51, v221, v195
	v_fmac_f32_e32 v43, v222, v195
	v_fmac_f32_e32 v65, v224, v79
	v_fmac_f32_e32 v62, v224, v80
	v_fmac_f32_e32 v63, v224, v81
	v_fmac_f32_e32 v57, v225, v79
	v_fmac_f32_e32 v54, v225, v80
	v_fmac_f32_e32 v55, v225, v81
	v_fmac_f32_e32 v49, v226, v79
	v_fmac_f32_e32 v46, v226, v80
	v_fmac_f32_e32 v47, v226, v81
	ds_read_b128 v[228:231], v236 offset:896
	v_fmac_f32_e32 v61, v224, v189
	v_fmac_f32_e32 v58, v224, v190
	v_fmac_f32_e32 v59, v224, v191
	v_fmac_f32_e32 v53, v225, v189
	v_fmac_f32_e32 v50, v225, v190
	v_fmac_f32_e32 v51, v225, v191
	v_fmac_f32_e32 v45, v226, v189
	v_fmac_f32_e32 v42, v226, v190
	v_fmac_f32_e32 v43, v226, v191
	ds_read_b128 v[232:235], v236 offset:960
	s_waitcnt vmcnt(1)
	v_cvt_pk_f32_fp8_e32 v[192:193], v33
	v_cvt_pk_f32_fp8_sdwa v[194:195], v33 src0_sel:WORD_1
	s_waitcnt lgkmcnt(1)
	v_cvt_pk_f32_fp8_e32 v[78:79], v32
	v_cvt_pk_f32_fp8_sdwa v[80:81], v32 src0_sel:WORD_1
	v_fmac_f32_e32 v64, v228, v78
	v_fmac_f32_e32 v65, v228, v79
	v_fmac_f32_e32 v62, v228, v80
	v_fmac_f32_e32 v63, v228, v81
	v_fmac_f32_e32 v60, v228, v192
	v_fmac_f32_e32 v61, v228, v193
	v_fmac_f32_e32 v58, v228, v194
	v_fmac_f32_e32 v59, v228, v195
	v_fmac_f32_e32 v56, v229, v78
	v_fmac_f32_e32 v57, v229, v79
	v_fmac_f32_e32 v54, v229, v80
	v_fmac_f32_e32 v55, v229, v81
	v_fmac_f32_e32 v52, v229, v192
	v_fmac_f32_e32 v53, v229, v193
	v_fmac_f32_e32 v50, v229, v194
	v_fmac_f32_e32 v51, v229, v195
	v_fmac_f32_e32 v48, v230, v78
	v_fmac_f32_e32 v49, v230, v79
	v_fmac_f32_e32 v46, v230, v80
	v_fmac_f32_e32 v47, v230, v81
	v_fmac_f32_e32 v44, v230, v192
	v_fmac_f32_e32 v45, v230, v193
	v_fmac_f32_e32 v42, v230, v194
	v_fmac_f32_e32 v43, v230, v195
	v_fmac_f32_e32 v40, v231, v78
	v_fmac_f32_e32 v41, v231, v79
	v_fmac_f32_e32 v38, v231, v80
	v_fmac_f32_e32 v39, v231, v81
	v_fmac_f32_e32 v36, v231, v192
	v_fmac_f32_e32 v37, v231, v193
	v_fmac_f32_e32 v26, v231, v194
	v_fmac_f32_e32 v27, v231, v195
	s_waitcnt vmcnt(0)
	v_cvt_pk_f32_fp8_e32 v[78:79], v34
	v_cvt_pk_f32_fp8_sdwa v[80:81], v34 src0_sel:WORD_1
	s_waitcnt lgkmcnt(0)
	v_cvt_pk_f32_fp8_e32 v[188:189], v35
	v_cvt_pk_f32_fp8_sdwa v[190:191], v35 src0_sel:WORD_1
	v_fmac_f32_e32 v64, v232, v78
	v_fmac_f32_e32 v65, v232, v79
	v_fmac_f32_e32 v62, v232, v80
	v_fmac_f32_e32 v63, v232, v81
	v_fmac_f32_e32 v60, v232, v188
	v_fmac_f32_e32 v61, v232, v189
	v_fmac_f32_e32 v58, v232, v190
	v_fmac_f32_e32 v59, v232, v191
	v_fmac_f32_e32 v56, v233, v78
	v_fmac_f32_e32 v57, v233, v79
	v_fmac_f32_e32 v54, v233, v80
	v_fmac_f32_e32 v55, v233, v81
	v_fmac_f32_e32 v52, v233, v188
	v_fmac_f32_e32 v53, v233, v189
	v_fmac_f32_e32 v50, v233, v190
	v_fmac_f32_e32 v51, v233, v191
	v_fmac_f32_e32 v48, v234, v78
	v_fmac_f32_e32 v49, v234, v79
	v_fmac_f32_e32 v46, v234, v80
	v_fmac_f32_e32 v47, v234, v81
	v_fmac_f32_e32 v44, v234, v188
	v_fmac_f32_e32 v45, v234, v189
	v_fmac_f32_e32 v42, v234, v190
	v_fmac_f32_e32 v43, v234, v191
	v_fmac_f32_e32 v40, v235, v78
	v_fmac_f32_e32 v41, v235, v79
	v_fmac_f32_e32 v38, v235, v80
	v_fmac_f32_e32 v39, v235, v81
	v_fmac_f32_e32 v36, v235, v188
	v_fmac_f32_e32 v37, v235, v189
	v_fmac_f32_e32 v26, v235, v190
	v_fmac_f32_e32 v27, v235, v191
	s_andn2_b64 vcc, exec, s[14:15]
	s_cbranch_vccnz .LBB0_1243
	s_cmp_ge_u32 s16, s3
	s_cbranch_scc1 .LBB0_1242
	v_lshl_add_u32 v237, v74, 1, v84
	ds_read_u16 v2, v237 offset:33024
	ds_read_u16 v10, v237 offset:33032
	ds_read_u16 v11, v237 offset:33040
	ds_read_u16 v12, v237 offset:33048
	ds_read_u16 v13, v237 offset:33056
	ds_read_u16 v14, v237 offset:33064
	ds_read_u16 v15, v237 offset:33072
	ds_read_u16 v16, v237 offset:33080
	s_waitcnt lgkmcnt(7)
	v_lshlrev_b32_e32 v86, 9, v2
	v_lshl_add_u64 v[2:3], v[118:119], 0, v[86:87]
	s_waitcnt lgkmcnt(6)
	v_lshlrev_b32_e32 v86, 9, v10
	v_lshl_add_u64 v[4:5], v[118:119], 0, v[86:87]
	s_waitcnt lgkmcnt(5)
	v_lshlrev_b32_e32 v86, 9, v11
	v_lshl_add_u64 v[6:7], v[118:119], 0, v[86:87]
	s_waitcnt lgkmcnt(4)
	v_lshlrev_b32_e32 v86, 9, v12
	v_lshl_add_u64 v[8:9], v[118:119], 0, v[86:87]
	s_waitcnt lgkmcnt(3)
	v_lshlrev_b32_e32 v86, 9, v13
	v_lshl_add_u64 v[10:11], v[118:119], 0, v[86:87]
	s_waitcnt lgkmcnt(2)
	v_lshlrev_b32_e32 v86, 9, v14
	v_lshl_add_u64 v[12:13], v[118:119], 0, v[86:87]
	s_waitcnt lgkmcnt(1)
	v_lshlrev_b32_e32 v86, 9, v15
	v_lshl_add_u64 v[14:15], v[118:119], 0, v[86:87]
	s_waitcnt lgkmcnt(0)
	v_lshlrev_b32_e32 v86, 9, v16
	v_lshl_add_u64 v[16:17], v[118:119], 0, v[86:87]
	global_load_dwordx2 v[2:3], v[2:3], off offset:128
	s_nop 0
	global_load_dwordx2 v[4:5], v[4:5], off offset:128
	s_nop 0
	global_load_dwordx2 v[6:7], v[6:7], off offset:128
	s_nop 0
	global_load_dwordx2 v[8:9], v[8:9], off offset:128
	s_nop 0
	global_load_dwordx2 v[10:11], v[10:11], off offset:128
	s_nop 0
	global_load_dwordx2 v[12:13], v[12:13], off offset:128
	s_nop 0
	global_load_dwordx2 v[14:15], v[14:15], off offset:128
	s_nop 0
	global_load_dwordx2 v[16:17], v[16:17], off offset:128
	ds_read_u16 v18, v237 offset:33088
	ds_read_u16 v28, v237 offset:33096
	ds_read_u16 v29, v237 offset:33104
	ds_read_u16 v30, v237 offset:33112
	ds_read_u16 v31, v237 offset:33120
	ds_read_u16 v32, v237 offset:33128
	ds_read_u16 v33, v237 offset:33136
	ds_read_u16 v34, v237 offset:33144
	s_waitcnt lgkmcnt(7)
	v_lshlrev_b32_e32 v86, 9, v18
	v_lshl_add_u64 v[18:19], v[118:119], 0, v[86:87]
	s_waitcnt lgkmcnt(6)
	v_lshlrev_b32_e32 v86, 9, v28
	v_lshl_add_u64 v[20:21], v[118:119], 0, v[86:87]
	s_waitcnt lgkmcnt(5)
	v_lshlrev_b32_e32 v86, 9, v29
	v_lshl_add_u64 v[22:23], v[118:119], 0, v[86:87]
	s_waitcnt lgkmcnt(4)
	v_lshlrev_b32_e32 v86, 9, v30
	v_lshl_add_u64 v[24:25], v[118:119], 0, v[86:87]
	s_waitcnt lgkmcnt(3)
	v_lshlrev_b32_e32 v86, 9, v31
	v_lshl_add_u64 v[28:29], v[118:119], 0, v[86:87]
	s_waitcnt lgkmcnt(2)
	v_lshlrev_b32_e32 v86, 9, v32
	v_lshl_add_u64 v[30:31], v[118:119], 0, v[86:87]
	s_waitcnt lgkmcnt(1)
	v_lshlrev_b32_e32 v86, 9, v33
	v_lshl_add_u64 v[32:33], v[118:119], 0, v[86:87]
	s_waitcnt lgkmcnt(0)
	v_lshlrev_b32_e32 v86, 9, v34
	v_lshl_add_u64 v[34:35], v[118:119], 0, v[86:87]
	global_load_dwordx2 v[18:19], v[18:19], off offset:128
	s_nop 0
	global_load_dwordx2 v[20:21], v[20:21], off offset:128
	s_nop 0
	global_load_dwordx2 v[22:23], v[22:23], off offset:128
	s_nop 0
	global_load_dwordx2 v[24:25], v[24:25], off offset:128
	s_nop 0
	global_load_dwordx2 v[28:29], v[28:29], off offset:128
	s_nop 0
	global_load_dwordx2 v[30:31], v[30:31], off offset:128
	s_nop 0
	global_load_dwordx2 v[32:33], v[32:33], off offset:128
	s_nop 0
	global_load_dwordx2 v[34:35], v[34:35], off offset:128

	.amdhsa_kernel _Z10fwd_kernel6Params
		.amdhsa_group_segment_fixed_size 0
		.amdhsa_private_segment_fixed_size 0
		.amdhsa_kernarg_size 464
		.amdhsa_user_sgpr_count 2
		.amdhsa_user_sgpr_dispatch_ptr 0
		.amdhsa_user_sgpr_queue_ptr 0
		.amdhsa_user_sgpr_kernarg_segment_ptr 1
		.amdhsa_user_sgpr_dispatch_id 0
		.amdhsa_user_sgpr_kernarg_preload_length 0
		.amdhsa_user_sgpr_kernarg_preload_offset 0
		.amdhsa_user_sgpr_private_segment_size 0
		.amdhsa_uses_dynamic_stack 0
		.amdhsa_enable_private_segment 0
		.amdhsa_system_sgpr_workgroup_id_x 1
		.amdhsa_system_sgpr_workgroup_id_y 0
		.amdhsa_system_sgpr_workgroup_id_z 0
		.amdhsa_system_sgpr_workgroup_info 0
		.amdhsa_system_vgpr_workitem_id 0
		.amdhsa_next_free_vgpr 256
		.amdhsa_next_free_sgpr 102
		.amdhsa_accum_offset 256
		.amdhsa_reserve_vcc 1
		.amdhsa_float_round_mode_32 0
		.amdhsa_float_round_mode_16_64 0
		.amdhsa_float_denorm_mode_32 3
		.amdhsa_float_denorm_mode_16_64 3
		.amdhsa_dx10_clamp 1
		.amdhsa_ieee_mode 1
		.amdhsa_fp16_overflow 0
		.amdhsa_tg_split 0
		.amdhsa_exception_fp_ieee_invalid_op 0
		.amdhsa_exception_fp_denorm_src 0
		.amdhsa_exception_fp_ieee_div_zero 0
		.amdhsa_exception_fp_ieee_overflow 0
		.amdhsa_exception_fp_ieee_underflow 0
		.amdhsa_exception_fp_ieee_inexact 0
		.amdhsa_exception_int_div_zero 0
	.end_amdhsa_kernel

amdhsa.kernels:
  - .agpr_count:     0
    .args:
      - .offset:         0
        .size:           208
        .value_kind:     by_value
      - .offset:         208
        .size:           4
        .value_kind:     hidden_block_count_x
      - .offset:         212
        .size:           4
        .value_kind:     hidden_block_count_y
      - .offset:         216
        .size:           4
        .value_kind:     hidden_block_count_z
      - .offset:         220
        .size:           2
        .value_kind:     hidden_group_size_x
      - .offset:         222
        .size:           2
        .value_kind:     hidden_group_size_y
      - .offset:         224
        .size:           2
        .value_kind:     hidden_group_size_z
      - .offset:         226
        .size:           2
        .value_kind:     hidden_remainder_x
      - .offset:         228
        .size:           2
        .value_kind:     hidden_remainder_y
      - .offset:         230
        .size:           2
        .value_kind:     hidden_remainder_z
      - .offset:         248
        .size:           8
        .value_kind:     hidden_global_offset_x
      - .offset:         256
        .size:           8
        .value_kind:     hidden_global_offset_y
      - .offset:         264
        .size:           8
        .value_kind:     hidden_global_offset_z
      - .offset:         272
        .size:           2
        .value_kind:     hidden_grid_dims
      - .offset:         328
        .size:           4
        .value_kind:     hidden_dynamic_lds_size
    .group_segment_fixed_size: 0
    .kernarg_segment_align: 8
    .kernarg_segment_size: 464
    .language:       OpenCL C
    .language_version:
      - 2
      - 0
    .max_flat_workgroup_size: 512
    .name:           _Z10fwd_kernel6Params
    .private_segment_fixed_size: 0
    .sgpr_count:     108
    .sgpr_spill_count: 76
    .symbol:         _Z10fwd_kernel6Params.kd
    .uniform_work_group_size: 1
    .uses_dynamic_stack: false
    .vgpr_count:     256
    .vgpr_spill_count: 0
    .wavefront_size: 64
